# non-temporal hint on read-once loads (attention query rows, LN1/final row + slot + expert-choice loads) and on the final output stores
# speedup vs baseline: 1.0062x; 1.0003x over previous
; #define LAS __attribute__((address_space(3)))
; DI void attn_unit(const Args& A, LAS unsigned char* lds, int unit, int tid, int wave, int lane) {
;     const bf16* Z = (const bf16*)(A.ws + WS_Z); bf16* ao = (bf16*)(A.ws + WS_ATTO); float* al = (float*)(A.ws + WS_ATTL);
;     const int x = unit & 15; int r0 = unit >> 4; const int hh = r0 & 3; r0 >>= 2; const int b = r0 % NB, br = r0 / NB;
;     const int dil = br == 0 ? 1 : (br == 1 ? 4 : 16), lsub = SEQ / dil, nblk = lsub / 128;
;     const int res = x / nblk, nbk = x % nblk, l0 = nbk * 128, wbase = l0 - 64;
;     LAS bf16* Qs = (LAS bf16*)(lds + AT_QS); LAS bf16* Ks = (LAS bf16*)(lds + AT_KS); LAS bf16* Vt = (LAS bf16*)(lds + AT_VT); LAS float* btab = (LAS float*)(lds + AT_BT);
;     __syncthreads();
; #pragma unroll
;     for (int i = 0; i < 2; ++i) { const int id = tid + 512 * i, row = id >> 3, ch = id & 7; const int tok = b * SEQ + (l0 + row) * dil + res;
;         *(LAS u32x4_t*)(Qs + row * AT_QLD + ch * 8) = *(const u32x4_t*)(Z + (size_t)tok * ZLD + ZA + hh * 64 + ch * 8); }
;     for (int id = tid; id < 272 * 8; id += NTHR) { const int row = id >> 3, ch = id & 7; const int pos = wbase + row; u32x4_t v = (u32x4_t){0u, 0u, 0u, 0u};
;         if (row < 256 && pos >= 0 && pos < lsub) v = *(const u32x4_t*)(Z + (size_t)(b * SEQ + pos * dil + res) * ZLD + ZA + 256 + hh * 64 + ch * 8);
;         *(LAS u32x4_t*)(Ks + row * AT_QLD + ch * 8) = v; }
;     for (int id = tid; id < 272 * 8; id += NTHR) { const int key = id % 272, ch = id / 272; const int pos = wbase + key; u32x4_t v = (u32x4_t){0u, 0u, 0u, 0u};
;         if (key < 256 && pos >= 0 && pos < lsub) v = *(const u32x4_t*)(Z + (size_t)(b * SEQ + pos * dil + res) * ZLD + ZA + 512 + hh * 64 + ch * 8);
;         LAS bf16* d = Vt + (ch * 8) * AT_VLD + key;
;         d[0] = (bf16)(v.x & 0xffffu); d[AT_VLD] = (bf16)(v.x >> 16); d[2 * AT_VLD] = (bf16)(v.y & 0xffffu); d[3 * AT_VLD] = (bf16)(v.y >> 16);
;         d[4 * AT_VLD] = (bf16)(v.z & 0xffffu); d[5 * AT_VLD] = (bf16)(v.z >> 16); d[6 * AT_VLD] = (bf16)(v.w & 0xffffu); d[7 * AT_VLD] = (bf16)(v.w >> 16); }
;     if (tid < 129) btab[tid] = A.in[I_RELB][t5_bucket((tid - 64) * dil) * 4 + hh] * 1.4426950408889634f;
;     __syncthreads();
.LBB0_244:
	s_cmp_lt_i32 s6, 4
	s_cselect_b64 s[0:1], -1, 0
	v_writelane_b32 v235, s0, 60
	s_nop 1
	v_writelane_b32 v235, s1, 61
	s_and_b64 s[0:1], s[0:1], s[2:3]
	s_andn2_b64 vcc, exec, s[0:1]
	v_writelane_b32 v235, s92, 62
	s_cbranch_vccnz .LBB0_496
	s_cmpk_gt_i32 s50, 0xa0
	s_cselect_b32 s0, 0x600, 0
	s_add_i32 s33, s0, s92
	s_cmpk_gt_i32 s33, 0x5ff
	s_mov_b32 s23, 0
	s_cbranch_scc1 .LBB0_336
	s_mov_b32 s6, s33
	s_mov_b32 s7, s50
	s_movk_i32 s8, 0x600
	v_readlane_b32 s9, v235, 52
	v_readlane_b32 s2, v235, 9
	v_readlane_b32 s3, v235, 10
	v_readlane_b32 s4, v235, 19
	v_readlane_b32 s5, v235, 20
	s_mov_b32 s72, 0x3e38aa3b
	s_mov_b32 s73, 0x3e38aa3b
	v_lshrrev_b32_e32 v2, 3, v0
	v_and_b32_e32 v3, 7, v0
	v_lshlrev_b32_e32 v3, 4, v3
	s_movk_i32 s39, 0x90
	v_mad_u32_u24 v1, v2, s39, v3
	v_and_b32_e32 v5, 0xff, v0
	v_lshrrev_b32_e32 v6, 8, v0
	s_movk_i32 s39, 0x1180
	v_mul_u32_u24_e32 v4, s39, v6
	v_lshl_add_u32 v4, v5, 1, v4
	v_add_u32_e32 v4, 0xe100, v4
	v_lshlrev_b32_e32 v6, 4, v6
	v_lshlrev_b32_e32 v8, 2, v5
	v_add_u32_e32 v8, 0x16d00, v8
	v_subrev_u32_e32 v165, 16, v0
	s_movk_i32 s39, 0x81
	v_cmp_gt_u32_e64 s[42:43], s39, v165
	s_movk_i32 s39, 0xa0
	v_cmp_gt_u32_e64 s[48:49], s39, v0
	v_cmp_gt_u32_e64 s[46:47], 64, v0
	v_cmp_gt_u32_e64 s[44:45], 16, v146
	v_subrev_u32_e32 v165, 0x50, v0
	v_cmp_lt_i32_e32 vcc, 0, v165
	v_mov_b32_e32 v7, 0
	s_nop 0
	v_cndmask_b32_e64 v166, 0, 16, vcc
	v_lshlrev_b32_e32 v167, 0, v165
	v_sub_u32_e32 v168, 0, v167
	v_max_i32_e32 v167, v167, v168
	v_cvt_f32_u32_e32 v168, v167
	v_mul_f32_e32 v168, 0x3e000000, v168
	v_max_f32_e32 v168, 1.0, v168
	v_log_f32_e32 v168, v168
	v_cmp_gt_u32_e32 vcc, 8, v167
	v_mul_f32_e32 v168, 0x3f924925, v168
	v_cvt_i32_f32_e32 v168, v168
	v_min_i32_e32 v168, 7, v168
	v_add_u32_e32 v168, 8, v168
	v_cndmask_b32_e32 v168, v168, v167, vcc
	v_add_u32_e32 v168, v168, v166
	v_lshl_or_b32 v7, v168, 0, v7
	v_lshlrev_b32_e32 v167, 2, v165
	v_sub_u32_e32 v168, 0, v167
	v_max_i32_e32 v167, v167, v168
	v_cvt_f32_u32_e32 v168, v167
	v_mul_f32_e32 v168, 0x3e000000, v168
	v_max_f32_e32 v168, 1.0, v168
	v_log_f32_e32 v168, v168
	v_cmp_gt_u32_e32 vcc, 8, v167
	v_mul_f32_e32 v168, 0x3f924925, v168
	v_cvt_i32_f32_e32 v168, v168
	v_min_i32_e32 v168, 7, v168
	v_add_u32_e32 v168, 8, v168
	v_cndmask_b32_e32 v168, v168, v167, vcc
	v_add_u32_e32 v168, v168, v166
	v_lshl_or_b32 v7, v168, 8, v7
	v_lshlrev_b32_e32 v167, 4, v165
	v_sub_u32_e32 v168, 0, v167
	v_max_i32_e32 v167, v167, v168
	v_cvt_f32_u32_e32 v168, v167
	v_mul_f32_e32 v168, 0x3e000000, v168
	v_max_f32_e32 v168, 1.0, v168
	v_log_f32_e32 v168, v168
	v_cmp_gt_u32_e32 vcc, 8, v167
	v_mul_f32_e32 v168, 0x3f924925, v168
	v_cvt_i32_f32_e32 v168, v168
	v_min_i32_e32 v168, 7, v168
	v_add_u32_e32 v168, 8, v168
	v_cndmask_b32_e32 v168, v168, v167, vcc
	v_add_u32_e32 v168, v168, v166
	v_lshl_or_b32 v7, v168, 16, v7
	v_and_b32_e32 v165, 15, v146
	v_lshrrev_b32_e32 v166, 4, v146
	s_lshl_b32 s39, s9, 4
	v_add_u32_e32 v40, s39, v165
	s_movk_i32 s40, 0x90
	v_mul_u32_u24_e32 v34, s40, v40
	v_lshl_add_u32 v34, v166, 4, v34
	v_lshlrev_b32_e32 v167, 2, v166
	v_sub_u32_e32 v35, v167, v165
	v_lshlrev_b32_e32 v35, 2, v35
	v_add_u32_e32 v35, 0x16d40, v35
	v_add_u32_e32 v167, s39, v167
	v_lshlrev_b32_e32 v36, 2, v167
	v_add_u32_e32 v36, 0x16f80, v36
	s_movk_i32 s40, 0x230
	v_mul_u32_u24_e32 v37, s40, v165
	v_lshl_add_u32 v37, v167, 1, v37
	v_add_u32_e32 v37, 0xe100, v37
	v_add_u32_e32 v9, 0x2300, v37
	v_add_u32_e32 v118, 0x4600, v37
	v_add_u32_e32 v144, 0x6900, v37
	v_xor_b32_e32 v38, 16, v146
	v_lshlrev_b32_e32 v38, 2, v38
	v_xor_b32_e32 v39, 32, v146
	v_lshlrev_b32_e32 v39, 2, v39
	v_lshlrev_b32_e32 v41, 3, v166
	v_mov_b32_e32 v232, 0
	v_mov_b32_e32 v233, 0
	s_movk_i32 s40, 0x230
	v_mul_u32_u24_e32 v168, s40, v0
	v_add_u32_e32 v168, 0xe300, v168
	s_and_saveexec_b64 s[40:41], s[46:47]
	ds_write_b64 v168, v[232:233] offset:0
	ds_write_b64 v168, v[232:233] offset:8
	ds_write_b64 v168, v[232:233] offset:16
	ds_write_b64 v168, v[232:233] offset:24
	s_mov_b64 exec, s[40:41]
	s_and_b32 s39, s6, 15
	s_bfe_u32 s40, s6, 0x20004
	s_bfe_u32 s41, s6, 0x30006
	s_lshr_b32 s74, s6, 9
	s_lshl_b32 s75, s74, 1
	s_lshl_b32 s16, 1536, s75
	s_add_i32 s20, s75, 9
	s_add_i32 s26, s75, 4
	s_lshl_b32 s28, s74, 3
	s_lshr_b32 s29, 0x800, s75
	s_add_i32 s17, s29, -1
	s_sub_i32 s76, 4, s75
	s_lshr_b32 s77, s39, s76
	s_lshr_b32 s78, 16, s75
	s_add_i32 s78, s78, -1
	s_and_b32 s78, s39, s78
	s_lshl_b32 s19, s78, 7
	s_add_i32 s18, s19, 0xffffffc0
	s_lshl_b32 s79, s41, 11
	s_add_i32 s79, s79, s77
	s_lshl_b32 s80, s40, 7
	s_lshl_b32 s27, s40, 2
	s_mul_i32 s81, s79, 1536
	s_add_u32 s81, s81, s80
	s_add_u32 s81, s81, 0x28600000
	s_add_u32 s10, s2, s81
	s_addc_u32 s11, s3, 0
	s_lshl_b32 s82, s74, 14
	s_add_i32 s82, s82, s79
	s_lshl_b32 s83, s82, 9
	s_add_u32 s83, s83, s80
	s_add_u32 s83, s83, 0x34a00000
	s_add_u32 s12, s2, s83
	s_addc_u32 s13, s3, 0
	s_lshl_b32 s84, s82, 4
	s_add_u32 s84, s84, s27
	s_add_u32 s84, s84, 0x36200000
	s_add_u32 s14, s2, s84
	s_addc_u32 s15, s3, 0
	v_add_u32_e32 v165, s19, v2
	v_mad_u32_u24 v165, v165, s16, v3
	s_lshl_b32 s85, s16, 6
	global_load_dwordx4 v[120:123], v165, s[10:11] nt
	v_add_u32_e32 v166, s85, v165
	global_load_dwordx4 v[124:127], v166, s[10:11] nt
	v_add_u32_e32 v167, s18, v2
	v_med3_i32 v168, v167, 0, s17
	v_mad_u32_u24 v168, v168, s16, v3
	global_load_dwordx4 v[128:131], v168, s[10:11] offset:512
	v_add_u32_e32 v168, 64, v167
	v_med3_i32 v168, v168, 0, s17
	v_mad_u32_u24 v168, v168, s16, v3
	global_load_dwordx4 v[132:135], v168, s[10:11] offset:512
	v_add_u32_e32 v168, 0x80, v167
	v_med3_i32 v168, v168, 0, s17
	v_mad_u32_u24 v168, v168, s16, v3
	global_load_dwordx4 v[136:139], v168, s[10:11] offset:512
	v_add_u32_e32 v168, 0xc0, v167
	v_med3_i32 v168, v168, 0, s17
	v_mad_u32_u24 v168, v168, s16, v3
	global_load_dwordx4 v[140:143], v168, s[10:11] offset:512
	v_add_u32_e32 v169, s18, v5
	v_med3_i32 v169, v169, 0, s17
	v_mad_u32_u24 v169, v169, s16, v6
	global_load_dwordx4 v[148:151], v169, s[10:11] offset:1024
	global_load_dwordx4 v[152:155], v169, s[10:11] offset:1056
	global_load_dwordx4 v[156:159], v169, s[10:11] offset:1088
	global_load_dwordx4 v[160:163], v169, s[10:11] offset:1120
	v_bfe_u32 v171, v7, s28, 8
	v_lshl_add_u32 v171, v171, 4, s27
	s_mov_b64 exec, s[42:43]
	global_load_dword v164, v171, s[4:5]
	s_mov_b64 exec, -1
; #define LAS __attribute__((address_space(3)))
; DI void attn_unit(const Args& A, LAS unsigned char* lds, int unit, int tid, int wave, int lane) {
;     ...
;     __syncthreads();
; #pragma unroll
;     for (int i = 0; i < 2; ++i) { const int id = tid + 512 * i, row = id >> 3, ch = id & 7; const int tok = b * SEQ + (l0 + row) * dil + res;
;         *(LAS u32x4_t*)(Qs + row * AT_QLD + ch * 8) = *(const u32x4_t*)(Z + (size_t)tok * ZLD + ZA + hh * 64 + ch * 8); }
;     for (int id = tid; id < 272 * 8; id += NTHR) { const int row = id >> 3, ch = id & 7; const int pos = wbase + row; u32x4_t v = (u32x4_t){0u, 0u, 0u, 0u};
;         if (row < 256 && pos >= 0 && pos < lsub) v = *(const u32x4_t*)(Z + (size_t)(b * SEQ + pos * dil + res) * ZLD + ZA + 256 + hh * 64 + ch * 8);
;         *(LAS u32x4_t*)(Ks + row * AT_QLD + ch * 8) = v; }
;     for (int id = tid; id < 272 * 8; id += NTHR) { const int key = id % 272, ch = id / 272; const int pos = wbase + key; u32x4_t v = (u32x4_t){0u, 0u, 0u, 0u};
;         if (key < 256 && pos >= 0 && pos < lsub) v = *(const u32x4_t*)(Z + (size_t)(b * SEQ + pos * dil + res) * ZLD + ZA + 512 + hh * 64 + ch * 8);
;         LAS bf16* d = Vt + (ch * 8) * AT_VLD + key;
;         d[0] = (bf16)(v.x & 0xffffu); d[AT_VLD] = (bf16)(v.x >> 16); d[2 * AT_VLD] = (bf16)(v.y & 0xffffu); d[3 * AT_VLD] = (bf16)(v.y >> 16);
;         d[4 * AT_VLD] = (bf16)(v.z & 0xffffu); d[5 * AT_VLD] = (bf16)(v.z >> 16); d[6 * AT_VLD] = (bf16)(v.w & 0xffffu); d[7 * AT_VLD] = (bf16)(v.w >> 16); }
;     if (tid < 129) btab[tid] = A.in[I_RELB][t5_bucket((tid - 64) * dil) * 4 + hh] * 1.4426950408889634f;
;     __syncthreads();
.LatA_loop:
	s_barrier
	s_mov_b64 s[30:31], s[12:13]
	s_mov_b64 s[32:33], s[14:15]
	s_mov_b32 s34, s19
	s_mov_b32 s35, s20
	s_mov_b32 s36, s26
	s_mov_b32 s37, s18
	s_mov_b32 s38, s29
	v_add_u32_e32 v165, s37, v5
	v_cmp_gt_u32_e32 vcc, s38, v165
	v_mov_b32_e32 v166, 0xf149f2ca
	s_nop 0
	v_cndmask_b32_e64 v165, v166, 0, vcc
	ds_write_b32 v8, v165 offset:640
	s_waitcnt vmcnt(0)
	ds_write_b128 v1, v[120:123]
	ds_write_b128 v1, v[124:127] offset:9216
	ds_write_b128 v1, v[128:131] offset:18432
	ds_write_b128 v1, v[132:135] offset:27648
	ds_write_b128 v1, v[136:139] offset:36864
	ds_write_b128 v1, v[140:143] offset:46080
	ds_write_b16 v4, v148 offset:0
	ds_write_b16_d16_hi v4, v148 offset:560
	ds_write_b16 v4, v149 offset:1120
	ds_write_b16_d16_hi v4, v149 offset:1680
	ds_write_b16 v4, v150 offset:2240
	ds_write_b16_d16_hi v4, v150 offset:2800
	ds_write_b16 v4, v151 offset:3360
	ds_write_b16_d16_hi v4, v151 offset:3920
	ds_write_b16 v4, v152 offset:8960
	ds_write_b16_d16_hi v4, v152 offset:9520
	ds_write_b16 v4, v153 offset:10080
	ds_write_b16_d16_hi v4, v153 offset:10640
	ds_write_b16 v4, v154 offset:11200
	ds_write_b16_d16_hi v4, v154 offset:11760
	ds_write_b16 v4, v155 offset:12320
	ds_write_b16_d16_hi v4, v155 offset:12880
	ds_write_b16 v4, v156 offset:17920
	ds_write_b16_d16_hi v4, v156 offset:18480
	ds_write_b16 v4, v157 offset:19040
	ds_write_b16_d16_hi v4, v157 offset:19600
	ds_write_b16 v4, v158 offset:20160
	ds_write_b16_d16_hi v4, v158 offset:20720
	ds_write_b16 v4, v159 offset:21280
	ds_write_b16_d16_hi v4, v159 offset:21840
	ds_write_b16 v4, v160 offset:26880
	ds_write_b16_d16_hi v4, v160 offset:27440
	ds_write_b16 v4, v161 offset:28000
	ds_write_b16_d16_hi v4, v161 offset:28560
	ds_write_b16 v4, v162 offset:29120
	ds_write_b16_d16_hi v4, v162 offset:29680
	ds_write_b16 v4, v163 offset:30240
	ds_write_b16_d16_hi v4, v163 offset:30800
	v_mul_f32_e32 v167, 0x3fb8aa3b, v164
	v_cndmask_b32_e64 v167, v166, v167, s[42:43]
	s_mov_b64 exec, s[48:49]
	ds_write_b32 v8, v167
	s_mov_b64 exec, -1
	s_add_i32 s6, s6, s7
	s_cmp_lt_i32 s6, s8
	s_cbranch_scc0 .LatA_nopf
	s_and_b32 s39, s6, 15
	s_bfe_u32 s40, s6, 0x20004
	s_bfe_u32 s41, s6, 0x30006
	s_lshr_b32 s74, s6, 9
	s_lshl_b32 s75, s74, 1
	s_lshl_b32 s16, 1536, s75
	s_add_i32 s20, s75, 9
	s_add_i32 s26, s75, 4
	s_lshl_b32 s28, s74, 3
	s_lshr_b32 s29, 0x800, s75
	s_add_i32 s17, s29, -1
	s_sub_i32 s76, 4, s75
	s_lshr_b32 s77, s39, s76
	s_lshr_b32 s78, 16, s75
	s_add_i32 s78, s78, -1
	s_and_b32 s78, s39, s78
	s_lshl_b32 s19, s78, 7
	s_add_i32 s18, s19, 0xffffffc0
	s_lshl_b32 s79, s41, 11
	s_add_i32 s79, s79, s77
	s_lshl_b32 s80, s40, 7
	s_lshl_b32 s27, s40, 2
	s_mul_i32 s81, s79, 1536
	s_add_u32 s81, s81, s80
	s_add_u32 s81, s81, 0x28600000
	s_add_u32 s10, s2, s81
	s_addc_u32 s11, s3, 0
	s_lshl_b32 s82, s74, 14
	s_add_i32 s82, s82, s79
	s_lshl_b32 s83, s82, 9
	s_add_u32 s83, s83, s80
	s_add_u32 s83, s83, 0x34a00000
	s_add_u32 s12, s2, s83
	s_addc_u32 s13, s3, 0
	s_lshl_b32 s84, s82, 4
	s_add_u32 s84, s84, s27
	s_add_u32 s84, s84, 0x36200000
	s_add_u32 s14, s2, s84
	s_addc_u32 s15, s3, 0
	v_add_u32_e32 v165, s19, v2
	v_mad_u32_u24 v165, v165, s16, v3
	s_lshl_b32 s85, s16, 6
	global_load_dwordx4 v[120:123], v165, s[10:11] nt
	v_add_u32_e32 v166, s85, v165
	global_load_dwordx4 v[124:127], v166, s[10:11] nt
	v_add_u32_e32 v167, s18, v2
	v_med3_i32 v168, v167, 0, s17
	v_mad_u32_u24 v168, v168, s16, v3
	global_load_dwordx4 v[128:131], v168, s[10:11] offset:512
	v_add_u32_e32 v168, 64, v167
	v_med3_i32 v168, v168, 0, s17
	v_mad_u32_u24 v168, v168, s16, v3
	global_load_dwordx4 v[132:135], v168, s[10:11] offset:512
	v_add_u32_e32 v168, 0x80, v167
	v_med3_i32 v168, v168, 0, s17
	v_mad_u32_u24 v168, v168, s16, v3
	global_load_dwordx4 v[136:139], v168, s[10:11] offset:512
	v_add_u32_e32 v168, 0xc0, v167
	v_med3_i32 v168, v168, 0, s17
	v_mad_u32_u24 v168, v168, s16, v3
	global_load_dwordx4 v[140:143], v168, s[10:11] offset:512
	v_add_u32_e32 v169, s18, v5
	v_med3_i32 v169, v169, 0, s17
	v_mad_u32_u24 v169, v169, s16, v6
	global_load_dwordx4 v[148:151], v169, s[10:11] offset:1024
	global_load_dwordx4 v[152:155], v169, s[10:11] offset:1056
	global_load_dwordx4 v[156:159], v169, s[10:11] offset:1088
	global_load_dwordx4 v[160:163], v169, s[10:11] offset:1120
	v_bfe_u32 v171, v7, s28, 8
	v_lshl_add_u32 v171, v171, 4, s27
	s_mov_b64 exec, s[42:43]
	global_load_dword v164, v171, s[4:5]
	s_mov_b64 exec, -1

; #define LAS __attribute__((address_space(3)))
; DI void attn_unit(const Args& A, LAS unsigned char* lds, int unit, int tid, int wave, int lane) {
;     const bf16* Z = (const bf16*)(A.ws + WS_Z); bf16* ao = (bf16*)(A.ws + WS_ATTO); float* al = (float*)(A.ws + WS_ATTL);
;     const int x = unit & 15; int r0 = unit >> 4; const int hh = r0 & 3; r0 >>= 2; const int b = r0 % NB, br = r0 / NB;
;     const int dil = br == 0 ? 1 : (br == 1 ? 4 : 16), lsub = SEQ / dil, nblk = lsub / 128;
;     const int res = x / nblk, nbk = x % nblk, l0 = nbk * 128, wbase = l0 - 64;
;     LAS bf16* Qs = (LAS bf16*)(lds + AT_QS); LAS bf16* Ks = (LAS bf16*)(lds + AT_KS); LAS bf16* Vt = (LAS bf16*)(lds + AT_VT); LAS float* btab = (LAS float*)(lds + AT_BT);
;     __syncthreads();
; #pragma unroll
;     for (int i = 0; i < 2; ++i) { const int id = tid + 512 * i, row = id >> 3, ch = id & 7; const int tok = b * SEQ + (l0 + row) * dil + res;
;         *(LAS u32x4_t*)(Qs + row * AT_QLD + ch * 8) = *(const u32x4_t*)(Z + (size_t)tok * ZLD + ZA + hh * 64 + ch * 8); }
;     for (int id = tid; id < 272 * 8; id += NTHR) { const int row = id >> 3, ch = id & 7; const int pos = wbase + row; u32x4_t v = (u32x4_t){0u, 0u, 0u, 0u};
;         if (row < 256 && pos >= 0 && pos < lsub) v = *(const u32x4_t*)(Z + (size_t)(b * SEQ + pos * dil + res) * ZLD + ZA + 256 + hh * 64 + ch * 8);
;         *(LAS u32x4_t*)(Ks + row * AT_QLD + ch * 8) = v; }
;     for (int id = tid; id < 272 * 8; id += NTHR) { const int key = id % 272, ch = id / 272; const int pos = wbase + key; u32x4_t v = (u32x4_t){0u, 0u, 0u, 0u};
;         if (key < 256 && pos >= 0 && pos < lsub) v = *(const u32x4_t*)(Z + (size_t)(b * SEQ + pos * dil + res) * ZLD + ZA + 512 + hh * 64 + ch * 8);
;         LAS bf16* d = Vt + (ch * 8) * AT_VLD + key;
;         d[0] = (bf16)(v.x & 0xffffu); d[AT_VLD] = (bf16)(v.x >> 16); d[2 * AT_VLD] = (bf16)(v.y & 0xffffu); d[3 * AT_VLD] = (bf16)(v.y >> 16);
;         d[4 * AT_VLD] = (bf16)(v.z & 0xffffu); d[5 * AT_VLD] = (bf16)(v.z >> 16); d[6 * AT_VLD] = (bf16)(v.w & 0xffffu); d[7 * AT_VLD] = (bf16)(v.w >> 16); }
;     if (tid < 129) btab[tid] = A.in[I_RELB][t5_bucket((tid - 64) * dil) * 4 + hh] * 1.4426950408889634f;
;     __syncthreads();
.Latmap_s22:
	v_readlane_b32 s9, v235, 52
	v_readlane_b32 s2, v235, 9
	v_readlane_b32 s3, v235, 10
	v_readlane_b32 s4, v235, 19
	v_readlane_b32 s5, v235, 20
	s_mov_b32 s72, 0x3e38aa3b
	s_mov_b32 s73, 0x3e38aa3b
	v_lshrrev_b32_e32 v2, 3, v0
	v_and_b32_e32 v3, 7, v0
	v_lshlrev_b32_e32 v3, 4, v3
	s_movk_i32 s39, 0x90
	v_mad_u32_u24 v1, v2, s39, v3
	v_and_b32_e32 v5, 0xff, v0
	v_lshrrev_b32_e32 v6, 8, v0
	s_movk_i32 s39, 0x1180
	v_mul_u32_u24_e32 v4, s39, v6
	v_lshl_add_u32 v4, v5, 1, v4
	v_add_u32_e32 v4, 0xe100, v4
	v_lshlrev_b32_e32 v6, 4, v6
	v_lshlrev_b32_e32 v8, 2, v5
	v_add_u32_e32 v8, 0x16d00, v8
	v_subrev_u32_e32 v165, 16, v0
	s_movk_i32 s39, 0x81
	v_cmp_gt_u32_e64 s[42:43], s39, v165
	s_movk_i32 s39, 0xa0
	v_cmp_gt_u32_e64 s[48:49], s39, v0
	v_cmp_gt_u32_e64 s[46:47], 64, v0
	v_cmp_gt_u32_e64 s[44:45], 16, v146
	v_subrev_u32_e32 v165, 0x50, v0
	v_cmp_lt_i32_e32 vcc, 0, v165
	v_mov_b32_e32 v7, 0
	s_nop 0
	v_cndmask_b32_e64 v166, 0, 16, vcc
	v_lshlrev_b32_e32 v167, 0, v165
	v_sub_u32_e32 v168, 0, v167
	v_max_i32_e32 v167, v167, v168
	v_cvt_f32_u32_e32 v168, v167
	v_mul_f32_e32 v168, 0x3e000000, v168
	v_max_f32_e32 v168, 1.0, v168
	v_log_f32_e32 v168, v168
	v_cmp_gt_u32_e32 vcc, 8, v167
	v_mul_f32_e32 v168, 0x3f924925, v168
	v_cvt_i32_f32_e32 v168, v168
	v_min_i32_e32 v168, 7, v168
	v_add_u32_e32 v168, 8, v168
	v_cndmask_b32_e32 v168, v168, v167, vcc
	v_add_u32_e32 v168, v168, v166
	v_lshl_or_b32 v7, v168, 0, v7
	v_lshlrev_b32_e32 v167, 2, v165
	v_sub_u32_e32 v168, 0, v167
	v_max_i32_e32 v167, v167, v168
	v_cvt_f32_u32_e32 v168, v167
	v_mul_f32_e32 v168, 0x3e000000, v168
	v_max_f32_e32 v168, 1.0, v168
	v_log_f32_e32 v168, v168
	v_cmp_gt_u32_e32 vcc, 8, v167
	v_mul_f32_e32 v168, 0x3f924925, v168
	v_cvt_i32_f32_e32 v168, v168
	v_min_i32_e32 v168, 7, v168
	v_add_u32_e32 v168, 8, v168
	v_cndmask_b32_e32 v168, v168, v167, vcc
	v_add_u32_e32 v168, v168, v166
	v_lshl_or_b32 v7, v168, 8, v7
	v_lshlrev_b32_e32 v167, 4, v165
	v_sub_u32_e32 v168, 0, v167
	v_max_i32_e32 v167, v167, v168
	v_cvt_f32_u32_e32 v168, v167
	v_mul_f32_e32 v168, 0x3e000000, v168
	v_max_f32_e32 v168, 1.0, v168
	v_log_f32_e32 v168, v168
	v_cmp_gt_u32_e32 vcc, 8, v167
	v_mul_f32_e32 v168, 0x3f924925, v168
	v_cvt_i32_f32_e32 v168, v168
	v_min_i32_e32 v168, 7, v168
	v_add_u32_e32 v168, 8, v168
	v_cndmask_b32_e32 v168, v168, v167, vcc
	v_add_u32_e32 v168, v168, v166
	v_lshl_or_b32 v7, v168, 16, v7
	v_and_b32_e32 v165, 15, v146
	v_lshrrev_b32_e32 v166, 4, v146
	s_lshl_b32 s39, s9, 4
	v_add_u32_e32 v40, s39, v165
	s_movk_i32 s40, 0x90
	v_mul_u32_u24_e32 v34, s40, v40
	v_lshl_add_u32 v34, v166, 4, v34
	v_lshlrev_b32_e32 v167, 2, v166
	v_sub_u32_e32 v35, v167, v165
	v_lshlrev_b32_e32 v35, 2, v35
	v_add_u32_e32 v35, 0x16d40, v35
	v_add_u32_e32 v167, s39, v167
	v_lshlrev_b32_e32 v36, 2, v167
	v_add_u32_e32 v36, 0x16f80, v36
	s_movk_i32 s40, 0x230
	v_mul_u32_u24_e32 v37, s40, v165
	v_lshl_add_u32 v37, v167, 1, v37
	v_add_u32_e32 v37, 0xe100, v37
	v_add_u32_e32 v9, 0x2300, v37
	v_add_u32_e32 v118, 0x4600, v37
	v_add_u32_e32 v144, 0x6900, v37
	v_xor_b32_e32 v38, 16, v146
	v_lshlrev_b32_e32 v38, 2, v38
	v_xor_b32_e32 v39, 32, v146
	v_lshlrev_b32_e32 v39, 2, v39
	v_lshlrev_b32_e32 v41, 3, v166
	v_mov_b32_e32 v232, 0
	v_mov_b32_e32 v233, 0
	s_movk_i32 s40, 0x230
	v_mul_u32_u24_e32 v168, s40, v0
	v_add_u32_e32 v168, 0xe300, v168
	s_and_saveexec_b64 s[40:41], s[46:47]
	ds_write_b64 v168, v[232:233] offset:0
	ds_write_b64 v168, v[232:233] offset:8
	ds_write_b64 v168, v[232:233] offset:16
	ds_write_b64 v168, v[232:233] offset:24
	s_mov_b64 exec, s[40:41]
	s_and_b32 s39, s6, 15
	s_bfe_u32 s40, s6, 0x20004
	s_bfe_u32 s41, s6, 0x30006
	s_lshr_b32 s74, s6, 9
	s_lshl_b32 s75, s74, 1
	s_lshl_b32 s16, 1536, s75
	s_add_i32 s20, s75, 9
	s_add_i32 s26, s75, 4
	s_lshl_b32 s28, s74, 3
	s_lshr_b32 s29, 0x800, s75
	s_add_i32 s17, s29, -1
	s_sub_i32 s76, 4, s75
	s_lshr_b32 s77, s39, s76
	s_lshr_b32 s78, 16, s75
	s_add_i32 s78, s78, -1
	s_and_b32 s78, s39, s78
	s_lshl_b32 s19, s78, 7
	s_add_i32 s18, s19, 0xffffffc0
	s_lshl_b32 s79, s41, 11
	s_add_i32 s79, s79, s77
	s_lshl_b32 s80, s40, 7
	s_lshl_b32 s27, s40, 2
	s_mul_i32 s81, s79, 1536
	s_add_u32 s81, s81, s80
	s_add_u32 s81, s81, 0x28600000
	s_add_u32 s10, s2, s81
	s_addc_u32 s11, s3, 0
	s_lshl_b32 s82, s74, 14
	s_add_i32 s82, s82, s79
	s_lshl_b32 s83, s82, 9
	s_add_u32 s83, s83, s80
	s_add_u32 s83, s83, 0x34a00000
	s_add_u32 s12, s2, s83
	s_addc_u32 s13, s3, 0
	s_lshl_b32 s84, s82, 4
	s_add_u32 s84, s84, s27
	s_add_u32 s84, s84, 0x36200000
	s_add_u32 s14, s2, s84
	s_addc_u32 s15, s3, 0
	v_add_u32_e32 v165, s19, v2
	v_mad_u32_u24 v165, v165, s16, v3
	s_lshl_b32 s85, s16, 6
	global_load_dwordx4 v[120:123], v165, s[10:11] nt
	v_add_u32_e32 v166, s85, v165
	global_load_dwordx4 v[124:127], v166, s[10:11] nt
	v_add_u32_e32 v167, s18, v2
	v_med3_i32 v168, v167, 0, s17
	v_mad_u32_u24 v168, v168, s16, v3
	global_load_dwordx4 v[128:131], v168, s[10:11] offset:512
	v_add_u32_e32 v168, 64, v167
	v_med3_i32 v168, v168, 0, s17
	v_mad_u32_u24 v168, v168, s16, v3
	global_load_dwordx4 v[132:135], v168, s[10:11] offset:512
	v_add_u32_e32 v168, 0x80, v167
	v_med3_i32 v168, v168, 0, s17
	v_mad_u32_u24 v168, v168, s16, v3
	global_load_dwordx4 v[136:139], v168, s[10:11] offset:512
	v_add_u32_e32 v168, 0xc0, v167
	v_med3_i32 v168, v168, 0, s17
	v_mad_u32_u24 v168, v168, s16, v3
	global_load_dwordx4 v[140:143], v168, s[10:11] offset:512
	v_add_u32_e32 v169, s18, v5
	v_med3_i32 v169, v169, 0, s17
	v_mad_u32_u24 v169, v169, s16, v6
	global_load_dwordx4 v[148:151], v169, s[10:11] offset:1024
	global_load_dwordx4 v[152:155], v169, s[10:11] offset:1056
	global_load_dwordx4 v[156:159], v169, s[10:11] offset:1088
	global_load_dwordx4 v[160:163], v169, s[10:11] offset:1120
	v_bfe_u32 v171, v7, s28, 8
	v_lshl_add_u32 v171, v171, 4, s27
	s_mov_b64 exec, s[42:43]
	global_load_dword v164, v171, s[4:5]
	s_mov_b64 exec, -1

; DI void add_slots(const Args& A, int tok, int lane, f32x4 (&v)[4]) {
;     const int* sel = (const int*)(A.ws + WS_SEL); const bf16* ys = (const bf16*)(A.ws + WS_YS);
;     const int b = tok / SEQ; const int mys = (lane < NE) ? sel[(size_t)tok * NE + lane] : -1;
;     unsigned m = (unsigned)__ballot(mys >= 0);
; DI void phase_ln1(const Args& A, int l, int gw, int ngw, int lane) {
;     const float* xin = A.in[I_X]; const bf16* x1 = (const bf16*)(A.ws + WS_X1); bf16* x2 = (bf16*)(A.ws + WS_X2); bf16* hb = (bf16*)(A.ws + WS_HB);
;     f32x4 gg[4];
; #pragma unroll
;     for (int j = 0; j < 4; ++j) gg[j] = ((const f32x4*)(A.in[I_LN1G] + (size_t)l * DM) + lane)[64 * j];
;     for (int tok = gw; tok < NT; tok += 2 * ngw) {
;         const int tokb = tok + ngw; const bool hb2 = tokb < NT;
;         f32x4 va[4], vb[4];
;         if (l == 0) { load_row(xin + (size_t)tok * DM, lane, va); load_row(xin + (size_t)(hb2 ? tokb : tok) * DM, lane, vb); }
;         else { load_row_bf(x1 + (size_t)tok * DM, lane, va); load_row_bf(x1 + (size_t)(hb2 ? tokb : tok) * DM, lane, vb);
;             add_slots(A, tok, lane, va); add_slots(A, hb2 ? tokb : tok, lane, vb);
.LBB0_1519:
	s_cmp_lt_i32 s10, 12
	s_cselect_b64 s[2:3], -1, 0
	s_and_b64 s[0:1], s[2:3], s[0:1]
	v_readlane_b32 s4, v235, 54
	v_readlane_b32 s5, v235, 55
	s_cmpk_lt_i32 s4, 0x4000
	s_cselect_b64 s[4:5], -1, 0
	v_writelane_b32 v234, s4, 42
	s_and_b64 s[0:1], s[0:1], s[4:5]
	s_andn2_b64 vcc, exec, s[0:1]
	v_writelane_b32 v234, s5, 43
	s_cbranch_vccnz .LBB0_1579
	s_cmpk_lg_i32 s50, 0x100
	s_cbranch_scc1 .Lrw1_orig
	s_waitcnt vmcnt(0) lgkmcnt(0)
	v_readlane_b32 s0, v235, 9
	v_readlane_b32 s1, v235, 10
	v_readlane_b32 s18, v235, 54
	v_readlane_b32 s20, v235, 21
	v_readlane_b32 s21, v235, 22
	v_lshlrev_b32_e32 v1, 3, v146
	v_lshlrev_b32_e32 v2, 2, v146
	v_lshlrev_b32_e32 v3, 4, v146
	v_xor_b32_e32 v4, 1, v146
	v_lshlrev_b32_e32 v4, 2, v4
	v_xor_b32_e32 v5, 2, v146
	v_lshlrev_b32_e32 v5, 2, v5
	v_xor_b32_e32 v6, 4, v146
	v_lshlrev_b32_e32 v6, 2, v6
	v_xor_b32_e32 v7, 8, v146
	v_lshlrev_b32_e32 v7, 2, v7
	v_xor_b32_e32 v8, 16, v146
	v_lshlrev_b32_e32 v8, 2, v8
	v_xor_b32_e32 v9, 32, v146
	v_lshlrev_b32_e32 v9, 2, v9
	v_mov_b32_e32 v171, 0x358637bd
	s_mov_b32 s39, 0x3a800000
	s_mov_b32 s40, 0x800000
	s_lshl_b32 s19, s18, 11
	s_add_u32 s4, s0, 0x22600000
	s_addc_u32 s5, s1, 0
	s_add_u32 s4, s4, s19
	s_addc_u32 s5, s5, 0
	s_lshl_b32 s34, s18, 6
	s_add_u32 s6, s0, 0x2c700000
	s_addc_u32 s7, s1, 0
	s_add_u32 s6, s6, s34
	s_addc_u32 s7, s7, 0
	s_add_u32 s12, s0, 0x3ba00000
	s_addc_u32 s13, s1, 0
	s_add_u32 s14, s0, 0x26600000
	s_addc_u32 s15, s1, 0
	s_add_u32 s14, s14, s19
	s_addc_u32 s15, s15, 0
	s_add_u32 s16, s0, 0x2a600000
	s_addc_u32 s17, s1, 0
	s_add_u32 s16, s16, s19
	s_addc_u32 s17, s17, 0
	s_add_u32 s20, s20, 0x1000
	s_addc_u32 s21, s21, 0
	v_mov_b32_e32 v10, -1
	v_mov_b32_e32 v11, -1
	v_mov_b32_e32 v12, -1
	v_mov_b32_e32 v13, -1
	v_mov_b32_e32 v14, -1
	v_mov_b32_e32 v15, -1
	v_mov_b32_e32 v16, -1
	v_mov_b32_e32 v17, -1
	s_mov_b64 exec, 0xffff
	s_mov_b64 s[34:35], s[6:7]
	global_load_dword v10, v2, s[34:35] nt
	s_add_u32 s34, s6, 0x20000
	s_addc_u32 s35, s7, 0
	global_load_dword v11, v2, s[34:35] nt
	s_add_u32 s34, s6, 0x40000
	s_addc_u32 s35, s7, 0
	global_load_dword v12, v2, s[34:35] nt
	s_add_u32 s34, s6, 0x60000
	s_addc_u32 s35, s7, 0
	global_load_dword v13, v2, s[34:35] nt
	s_add_u32 s34, s6, 0x80000
	s_addc_u32 s35, s7, 0
	global_load_dword v14, v2, s[34:35] nt
	s_add_u32 s34, s6, 0xa0000
	s_addc_u32 s35, s7, 0
	global_load_dword v15, v2, s[34:35] nt
	s_add_u32 s34, s6, 0xc0000
	s_addc_u32 s35, s7, 0
	global_load_dword v16, v2, s[34:35] nt
	s_add_u32 s34, s6, 0xe0000
	s_addc_u32 s35, s7, 0
	global_load_dword v17, v2, s[34:35] nt
	s_mov_b64 exec, -1
	s_mov_b64 s[34:35], s[4:5]
	global_load_dwordx2 v[34:35], v1, s[34:35] nt
	global_load_dwordx2 v[36:37], v1, s[34:35] offset:512 nt
	global_load_dwordx2 v[38:39], v1, s[34:35] offset:1024 nt
	global_load_dwordx2 v[40:41], v1, s[34:35] offset:1536 nt
	s_add_u32 s34, s4, 0x400000
	s_addc_u32 s35, s5, 0
	global_load_dwordx2 v[42:43], v1, s[34:35] nt
	global_load_dwordx2 v[44:45], v1, s[34:35] offset:512 nt
	global_load_dwordx2 v[46:47], v1, s[34:35] offset:1024 nt
	global_load_dwordx2 v[48:49], v1, s[34:35] offset:1536 nt
	s_add_u32 s34, s4, 0x800000
	s_addc_u32 s35, s5, 0
	global_load_dwordx2 v[50:51], v1, s[34:35] nt
	global_load_dwordx2 v[52:53], v1, s[34:35] offset:512 nt
	global_load_dwordx2 v[54:55], v1, s[34:35] offset:1024 nt
	global_load_dwordx2 v[56:57], v1, s[34:35] offset:1536 nt
	s_add_u32 s34, s4, 0xc00000
	s_addc_u32 s35, s5, 0
	global_load_dwordx2 v[58:59], v1, s[34:35] nt
	global_load_dwordx2 v[60:61], v1, s[34:35] offset:512 nt
	global_load_dwordx2 v[62:63], v1, s[34:35] offset:1024 nt
	global_load_dwordx2 v[64:65], v1, s[34:35] offset:1536 nt
	s_add_u32 s34, s4, 0x1000000
	s_addc_u32 s35, s5, 0
	global_load_dwordx2 v[66:67], v1, s[34:35] nt
	global_load_dwordx2 v[68:69], v1, s[34:35] offset:512 nt
	global_load_dwordx2 v[70:71], v1, s[34:35] offset:1024 nt
	global_load_dwordx2 v[72:73], v1, s[34:35] offset:1536 nt
	s_add_u32 s34, s4, 0x1400000
	s_addc_u32 s35, s5, 0
	global_load_dwordx2 v[74:75], v1, s[34:35] nt
	global_load_dwordx2 v[76:77], v1, s[34:35] offset:512 nt
	global_load_dwordx2 v[78:79], v1, s[34:35] offset:1024 nt
	global_load_dwordx2 v[80:81], v1, s[34:35] offset:1536 nt
	s_add_u32 s34, s4, 0x1800000
	s_addc_u32 s35, s5, 0
	global_load_dwordx2 v[82:83], v1, s[34:35] nt
	global_load_dwordx2 v[84:85], v1, s[34:35] offset:512 nt
	global_load_dwordx2 v[86:87], v1, s[34:35] offset:1024 nt
	global_load_dwordx2 v[88:89], v1, s[34:35] offset:1536 nt
	s_add_u32 s34, s4, 0x1c00000
	s_addc_u32 s35, s5, 0
	global_load_dwordx2 v[90:91], v1, s[34:35] nt
	global_load_dwordx2 v[92:93], v1, s[34:35] offset:512 nt
	global_load_dwordx2 v[94:95], v1, s[34:35] offset:1024 nt
	global_load_dwordx2 v[96:97], v1, s[34:35] offset:1536 nt
	global_load_dwordx4 v[18:21], v3, s[20:21]
	global_load_dwordx4 v[22:25], v3, s[20:21] offset:1024
	global_load_dwordx4 v[26:29], v3, s[20:21] offset:2048
	global_load_dwordx4 v[30:33], v3, s[20:21] offset:3072
	s_waitcnt vmcnt(36)
	v_cmp_le_i32_e64 s[66:67], 0, v10
	v_cmp_le_i32_e64 s[68:69], 0, v11
	v_cmp_le_i32_e64 s[70:71], 0, v12
	v_cmp_le_i32_e64 s[72:73], 0, v13
	v_cmp_le_i32_e64 s[74:75], 0, v14
	v_cmp_le_i32_e64 s[76:77], 0, v15
	v_cmp_le_i32_e64 s[78:79], 0, v16
	v_cmp_le_i32_e64 s[80:81], 0, v17
	s_nop 1
	s_mov_b32 s38, 1
; DI void add_slots(const Args& A, int tok, int lane, f32x4 (&v)[4]) {
;     ...
;     while (m) {
;         const uint2* p[4]; bool ok[4];
; #pragma unroll
;         for (int q = 0; q < 4; ++q) { ok[q] = m != 0u; const int e = ok[q] ? __builtin_ctz(m) : 0; m &= m - 1u; const int r = __shfl(mys, e);
;             p[q] = (const uint2*)(ys + (size_t)((e * NB + b) * CAP + (ok[q] ? r : 0)) * DM) + lane; }
;         uint2 w[4][4];
; #pragma unroll
;         for (int q = 0; q < 4; ++q) if (ok[q]) {
; #pragma unroll
;             for (int j = 0; j < 4; ++j) w[q][j] = p[q][64 * j]; }
.Lrw1_round0:
	s_mov_b32 s33, 0
	s_cmp_eq_u32 s66, 0
	s_cbranch_scc1 .Lrw1_i0_0
	s_ff1_i32_b32 s34, s66
	s_add_i32 s35, s66, -1
	s_and_b32 s66, s66, s35
	s_nop 1
	v_readlane_b32 s35, v10, s34
	s_lshl_b32 s34, s34, 22
	s_lshl_b32 s35, s35, 11
	s_add_u32 s34, s34, s35
	s_add_u32 s36, s12, s34
	s_addc_u32 s37, s13, 0
	global_load_dwordx2 v[98:99], v1, s[36:37] nt
	global_load_dwordx2 v[100:101], v1, s[36:37] offset:512 nt
	global_load_dwordx2 v[102:103], v1, s[36:37] offset:1024 nt
	global_load_dwordx2 v[104:105], v1, s[36:37] offset:1536 nt
	s_bitset1_b32 s33, 0
.Lrw1_i0_0:
	s_cmp_eq_u32 s66, 0
	s_cbranch_scc1 .Lrw1_i0_1
	s_ff1_i32_b32 s34, s66
	s_add_i32 s35, s66, -1
	s_and_b32 s66, s66, s35
	s_nop 1
	v_readlane_b32 s35, v10, s34
	s_lshl_b32 s34, s34, 22
	s_lshl_b32 s35, s35, 11
	s_add_u32 s34, s34, s35
	s_add_u32 s36, s12, s34
	s_addc_u32 s37, s13, 0
	global_load_dwordx2 v[106:107], v1, s[36:37] nt
	global_load_dwordx2 v[108:109], v1, s[36:37] offset:512 nt
	global_load_dwordx2 v[110:111], v1, s[36:37] offset:1024 nt
	global_load_dwordx2 v[112:113], v1, s[36:37] offset:1536 nt
	s_bitset1_b32 s33, 1
.Lrw1_i0_1:
	s_cmp_eq_u32 s68, 0
	s_cbranch_scc1 .Lrw1_i0_2
	s_ff1_i32_b32 s34, s68
	s_add_i32 s35, s68, -1
	s_and_b32 s68, s68, s35
	s_nop 1
	v_readlane_b32 s35, v11, s34
	s_lshl_b32 s34, s34, 22
	s_lshl_b32 s35, s35, 11
	s_add_u32 s34, s34, s35
	s_add_u32 s34, s34, 0x80000
	s_add_u32 s36, s12, s34
	s_addc_u32 s37, s13, 0
	global_load_dwordx2 v[114:115], v1, s[36:37] nt
	global_load_dwordx2 v[116:117], v1, s[36:37] offset:512 nt
	global_load_dwordx2 v[118:119], v1, s[36:37] offset:1024 nt
	global_load_dwordx2 v[148:149], v1, s[36:37] offset:1536 nt
	s_bitset1_b32 s33, 2
.Lrw1_i0_2:
	s_cmp_eq_u32 s68, 0
	s_cbranch_scc1 .Lrw1_i0_3
	s_ff1_i32_b32 s34, s68
	s_add_i32 s35, s68, -1
	s_and_b32 s68, s68, s35
	s_nop 1
	v_readlane_b32 s35, v11, s34
	s_lshl_b32 s34, s34, 22
	s_lshl_b32 s35, s35, 11
	s_add_u32 s34, s34, s35
	s_add_u32 s34, s34, 0x80000
	s_add_u32 s36, s12, s34
	s_addc_u32 s37, s13, 0
	global_load_dwordx2 v[150:151], v1, s[36:37] nt
	global_load_dwordx2 v[152:153], v1, s[36:37] offset:512 nt
	global_load_dwordx2 v[154:155], v1, s[36:37] offset:1024 nt
	global_load_dwordx2 v[156:157], v1, s[36:37] offset:1536 nt
	s_bitset1_b32 s33, 3
.Lrw1_i0_3:
	s_cmp_eq_u32 s70, 0
	s_cbranch_scc1 .Lrw1_i0_4
	s_ff1_i32_b32 s34, s70
	s_add_i32 s35, s70, -1
	s_and_b32 s70, s70, s35
	s_nop 1
	v_readlane_b32 s35, v12, s34
	s_lshl_b32 s34, s34, 22
	s_lshl_b32 s35, s35, 11
	s_add_u32 s34, s34, s35
	s_add_u32 s34, s34, 0x100000
	s_add_u32 s36, s12, s34
	s_addc_u32 s37, s13, 0
	global_load_dwordx2 v[158:159], v1, s[36:37] nt
	global_load_dwordx2 v[160:161], v1, s[36:37] offset:512 nt
	global_load_dwordx2 v[162:163], v1, s[36:37] offset:1024 nt
	global_load_dwordx2 v[164:165], v1, s[36:37] offset:1536 nt
	s_bitset1_b32 s33, 4
.Lrw1_i0_4:
	s_cmp_eq_u32 s70, 0
	s_cbranch_scc1 .Lrw1_i0_5
	s_ff1_i32_b32 s34, s70
	s_add_i32 s35, s70, -1
	s_and_b32 s70, s70, s35
	s_nop 1
	v_readlane_b32 s35, v12, s34
	s_lshl_b32 s34, s34, 22
	s_lshl_b32 s35, s35, 11
	s_add_u32 s34, s34, s35
	s_add_u32 s34, s34, 0x100000
	s_add_u32 s36, s12, s34
	s_addc_u32 s37, s13, 0
	global_load_dwordx2 v[166:167], v1, s[36:37] nt
	global_load_dwordx2 v[168:169], v1, s[36:37] offset:512 nt
	global_load_dwordx2 v[220:221], v1, s[36:37] offset:1024 nt
	global_load_dwordx2 v[222:223], v1, s[36:37] offset:1536 nt
	s_bitset1_b32 s33, 5
.Lrw1_i0_5:
	s_cmp_eq_u32 s72, 0
	s_cbranch_scc1 .Lrw1_i0_6
	s_ff1_i32_b32 s34, s72
	s_add_i32 s35, s72, -1
	s_and_b32 s72, s72, s35
	s_nop 1
	v_readlane_b32 s35, v13, s34
	s_lshl_b32 s34, s34, 22
	s_lshl_b32 s35, s35, 11
	s_add_u32 s34, s34, s35
	s_add_u32 s34, s34, 0x180000
	s_add_u32 s36, s12, s34
	s_addc_u32 s37, s13, 0
	global_load_dwordx2 v[224:225], v1, s[36:37] nt
	global_load_dwordx2 v[226:227], v1, s[36:37] offset:512 nt
	global_load_dwordx2 v[228:229], v1, s[36:37] offset:1024 nt
	global_load_dwordx2 v[230:231], v1, s[36:37] offset:1536 nt
	s_bitset1_b32 s33, 6
.Lrw1_i0_6:
	s_cmp_eq_u32 s72, 0
	s_cbranch_scc1 .Lrw1_i0_7
	s_ff1_i32_b32 s34, s72
	s_add_i32 s35, s72, -1
	s_and_b32 s72, s72, s35
	s_nop 1
	v_readlane_b32 s35, v13, s34
	s_lshl_b32 s34, s34, 22
	s_lshl_b32 s35, s35, 11
	s_add_u32 s34, s34, s35
	s_add_u32 s34, s34, 0x180000
	s_add_u32 s36, s12, s34
	s_addc_u32 s37, s13, 0
	global_load_dwordx2 v[232:233], v1, s[36:37] nt
	global_load_dwordx2 v[140:141], v1, s[36:37] offset:512 nt
	global_load_dwordx2 v[142:143], v1, s[36:37] offset:1024 nt
	global_load_dwordx2 v[144:145], v1, s[36:37] offset:1536 nt
	s_bitset1_b32 s33, 7

; DI void add_slots(const Args& A, int tok, int lane, f32x4 (&v)[4]) {
;     ...
;     while (m) {
;         const uint2* p[4]; bool ok[4];
; #pragma unroll
;         for (int q = 0; q < 4; ++q) { ok[q] = m != 0u; const int e = ok[q] ? __builtin_ctz(m) : 0; m &= m - 1u; const int r = __shfl(mys, e);
;             p[q] = (const uint2*)(ys + (size_t)((e * NB + b) * CAP + (ok[q] ? r : 0)) * DM) + lane; }
;         uint2 w[4][4];
; #pragma unroll
;         for (int q = 0; q < 4; ++q) if (ok[q]) {
; #pragma unroll
;             for (int j = 0; j < 4; ++j) w[q][j] = p[q][64 * j]; }
.Lrw1_round1:
	s_mov_b32 s33, 0
	s_cmp_eq_u32 s74, 0
	s_cbranch_scc1 .Lrw1_i1_0
	s_ff1_i32_b32 s34, s74
	s_add_i32 s35, s74, -1
	s_and_b32 s74, s74, s35
	s_nop 1
	v_readlane_b32 s35, v14, s34
	s_lshl_b32 s34, s34, 22
	s_lshl_b32 s35, s35, 11
	s_add_u32 s34, s34, s35
	s_add_u32 s34, s34, 0x200000
	s_add_u32 s36, s12, s34
	s_addc_u32 s37, s13, 0
	global_load_dwordx2 v[98:99], v1, s[36:37] nt
	global_load_dwordx2 v[100:101], v1, s[36:37] offset:512 nt
	global_load_dwordx2 v[102:103], v1, s[36:37] offset:1024 nt
	global_load_dwordx2 v[104:105], v1, s[36:37] offset:1536 nt
	s_bitset1_b32 s33, 0
.Lrw1_i1_0:
	s_cmp_eq_u32 s74, 0
	s_cbranch_scc1 .Lrw1_i1_1
	s_ff1_i32_b32 s34, s74
	s_add_i32 s35, s74, -1
	s_and_b32 s74, s74, s35
	s_nop 1
	v_readlane_b32 s35, v14, s34
	s_lshl_b32 s34, s34, 22
	s_lshl_b32 s35, s35, 11
	s_add_u32 s34, s34, s35
	s_add_u32 s34, s34, 0x200000
	s_add_u32 s36, s12, s34
	s_addc_u32 s37, s13, 0
	global_load_dwordx2 v[106:107], v1, s[36:37] nt
	global_load_dwordx2 v[108:109], v1, s[36:37] offset:512 nt
	global_load_dwordx2 v[110:111], v1, s[36:37] offset:1024 nt
	global_load_dwordx2 v[112:113], v1, s[36:37] offset:1536 nt
	s_bitset1_b32 s33, 1
.Lrw1_i1_1:
	s_cmp_eq_u32 s76, 0
	s_cbranch_scc1 .Lrw1_i1_2
	s_ff1_i32_b32 s34, s76
	s_add_i32 s35, s76, -1
	s_and_b32 s76, s76, s35
	s_nop 1
	v_readlane_b32 s35, v15, s34
	s_lshl_b32 s34, s34, 22
	s_lshl_b32 s35, s35, 11
	s_add_u32 s34, s34, s35
	s_add_u32 s34, s34, 0x280000
	s_add_u32 s36, s12, s34
	s_addc_u32 s37, s13, 0
	global_load_dwordx2 v[114:115], v1, s[36:37] nt
	global_load_dwordx2 v[116:117], v1, s[36:37] offset:512 nt
	global_load_dwordx2 v[118:119], v1, s[36:37] offset:1024 nt
	global_load_dwordx2 v[148:149], v1, s[36:37] offset:1536 nt
	s_bitset1_b32 s33, 2
.Lrw1_i1_2:
	s_cmp_eq_u32 s76, 0
	s_cbranch_scc1 .Lrw1_i1_3
	s_ff1_i32_b32 s34, s76
	s_add_i32 s35, s76, -1
	s_and_b32 s76, s76, s35
	s_nop 1
	v_readlane_b32 s35, v15, s34
	s_lshl_b32 s34, s34, 22
	s_lshl_b32 s35, s35, 11
	s_add_u32 s34, s34, s35
	s_add_u32 s34, s34, 0x280000
	s_add_u32 s36, s12, s34
	s_addc_u32 s37, s13, 0
	global_load_dwordx2 v[150:151], v1, s[36:37] nt
	global_load_dwordx2 v[152:153], v1, s[36:37] offset:512 nt
	global_load_dwordx2 v[154:155], v1, s[36:37] offset:1024 nt
	global_load_dwordx2 v[156:157], v1, s[36:37] offset:1536 nt
	s_bitset1_b32 s33, 3
.Lrw1_i1_3:
	s_cmp_eq_u32 s78, 0
	s_cbranch_scc1 .Lrw1_i1_4
	s_ff1_i32_b32 s34, s78
	s_add_i32 s35, s78, -1
	s_and_b32 s78, s78, s35
	s_nop 1
	v_readlane_b32 s35, v16, s34
	s_lshl_b32 s34, s34, 22
	s_lshl_b32 s35, s35, 11
	s_add_u32 s34, s34, s35
	s_add_u32 s34, s34, 0x300000
	s_add_u32 s36, s12, s34
	s_addc_u32 s37, s13, 0
	global_load_dwordx2 v[158:159], v1, s[36:37] nt
	global_load_dwordx2 v[160:161], v1, s[36:37] offset:512 nt
	global_load_dwordx2 v[162:163], v1, s[36:37] offset:1024 nt
	global_load_dwordx2 v[164:165], v1, s[36:37] offset:1536 nt
	s_bitset1_b32 s33, 4
.Lrw1_i1_4:
	s_cmp_eq_u32 s78, 0
	s_cbranch_scc1 .Lrw1_i1_5
	s_ff1_i32_b32 s34, s78
	s_add_i32 s35, s78, -1
	s_and_b32 s78, s78, s35
	s_nop 1
	v_readlane_b32 s35, v16, s34
	s_lshl_b32 s34, s34, 22
	s_lshl_b32 s35, s35, 11
	s_add_u32 s34, s34, s35
	s_add_u32 s34, s34, 0x300000
	s_add_u32 s36, s12, s34
	s_addc_u32 s37, s13, 0
	global_load_dwordx2 v[166:167], v1, s[36:37] nt
	global_load_dwordx2 v[168:169], v1, s[36:37] offset:512 nt
	global_load_dwordx2 v[220:221], v1, s[36:37] offset:1024 nt
	global_load_dwordx2 v[222:223], v1, s[36:37] offset:1536 nt
	s_bitset1_b32 s33, 5
.Lrw1_i1_5:
	s_cmp_eq_u32 s80, 0
	s_cbranch_scc1 .Lrw1_i1_6
	s_ff1_i32_b32 s34, s80
	s_add_i32 s35, s80, -1
	s_and_b32 s80, s80, s35
	s_nop 1
	v_readlane_b32 s35, v17, s34
	s_lshl_b32 s34, s34, 22
	s_lshl_b32 s35, s35, 11
	s_add_u32 s34, s34, s35
	s_add_u32 s34, s34, 0x380000
	s_add_u32 s36, s12, s34
	s_addc_u32 s37, s13, 0
	global_load_dwordx2 v[224:225], v1, s[36:37] nt
	global_load_dwordx2 v[226:227], v1, s[36:37] offset:512 nt
	global_load_dwordx2 v[228:229], v1, s[36:37] offset:1024 nt
	global_load_dwordx2 v[230:231], v1, s[36:37] offset:1536 nt
	s_bitset1_b32 s33, 6
.Lrw1_i1_6:
	s_cmp_eq_u32 s80, 0
	s_cbranch_scc1 .Lrw1_i1_7
	s_ff1_i32_b32 s34, s80
	s_add_i32 s35, s80, -1
	s_and_b32 s80, s80, s35
	s_nop 1
	v_readlane_b32 s35, v17, s34
	s_lshl_b32 s34, s34, 22
	s_lshl_b32 s35, s35, 11
	s_add_u32 s34, s34, s35
	s_add_u32 s34, s34, 0x380000
	s_add_u32 s36, s12, s34
	s_addc_u32 s37, s13, 0
	global_load_dwordx2 v[232:233], v1, s[36:37] nt
	global_load_dwordx2 v[140:141], v1, s[36:37] offset:512 nt
	global_load_dwordx2 v[142:143], v1, s[36:37] offset:1024 nt
	global_load_dwordx2 v[144:145], v1, s[36:37] offset:1536 nt
	s_bitset1_b32 s33, 7

; #define LAS __attribute__((address_space(3)))
; DI void attn_unit(const Args& A, LAS unsigned char* lds, int unit, int tid, int wave, int lane) {
;     const bf16* Z = (const bf16*)(A.ws + WS_Z); bf16* ao = (bf16*)(A.ws + WS_ATTO); float* al = (float*)(A.ws + WS_ATTL);
;     const int x = unit & 15; int r0 = unit >> 4; const int hh = r0 & 3; r0 >>= 2; const int b = r0 % NB, br = r0 / NB;
;     const int dil = br == 0 ? 1 : (br == 1 ? 4 : 16), lsub = SEQ / dil, nblk = lsub / 128;
;     const int res = x / nblk, nbk = x % nblk, l0 = nbk * 128, wbase = l0 - 64;
;     LAS bf16* Qs = (LAS bf16*)(lds + AT_QS); LAS bf16* Ks = (LAS bf16*)(lds + AT_KS); LAS bf16* Vt = (LAS bf16*)(lds + AT_VT); LAS float* btab = (LAS float*)(lds + AT_BT);
;     __syncthreads();
; #pragma unroll
;     for (int i = 0; i < 2; ++i) { const int id = tid + 512 * i, row = id >> 3, ch = id & 7; const int tok = b * SEQ + (l0 + row) * dil + res;
;         *(LAS u32x4_t*)(Qs + row * AT_QLD + ch * 8) = *(const u32x4_t*)(Z + (size_t)tok * ZLD + ZA + hh * 64 + ch * 8); }
;     for (int id = tid; id < 272 * 8; id += NTHR) { const int row = id >> 3, ch = id & 7; const int pos = wbase + row; u32x4_t v = (u32x4_t){0u, 0u, 0u, 0u};
;         if (row < 256 && pos >= 0 && pos < lsub) v = *(const u32x4_t*)(Z + (size_t)(b * SEQ + pos * dil + res) * ZLD + ZA + 256 + hh * 64 + ch * 8);
;         *(LAS u32x4_t*)(Ks + row * AT_QLD + ch * 8) = v; }
;     for (int id = tid; id < 272 * 8; id += NTHR) { const int key = id % 272, ch = id / 272; const int pos = wbase + key; u32x4_t v = (u32x4_t){0u, 0u, 0u, 0u};
;         if (key < 256 && pos >= 0 && pos < lsub) v = *(const u32x4_t*)(Z + (size_t)(b * SEQ + pos * dil + res) * ZLD + ZA + 512 + hh * 64 + ch * 8);
;         LAS bf16* d = Vt + (ch * 8) * AT_VLD + key;
;         d[0] = (bf16)(v.x & 0xffffu); d[AT_VLD] = (bf16)(v.x >> 16); d[2 * AT_VLD] = (bf16)(v.y & 0xffffu); d[3 * AT_VLD] = (bf16)(v.y >> 16);
;         d[4 * AT_VLD] = (bf16)(v.z & 0xffffu); d[5 * AT_VLD] = (bf16)(v.z >> 16); d[6 * AT_VLD] = (bf16)(v.w & 0xffffu); d[7 * AT_VLD] = (bf16)(v.w >> 16); }
;     if (tid < 129) btab[tid] = A.in[I_RELB][t5_bucket((tid - 64) * dil) * 4 + hh] * 1.4426950408889634f;
;     __syncthreads();
.LBB0_1704:
	s_cmp_lt_i32 s6, 14
	s_cselect_b64 s[0:1], -1, 0
	v_writelane_b32 v234, s0, 44
	s_nop 1
	v_writelane_b32 v234, s1, 45
	s_and_b64 s[0:1], s[0:1], s[2:3]
	s_andn2_b64 vcc, exec, s[0:1]
	s_cbranch_vccnz .LBB0_1958
	s_cmpk_gt_i32 s50, 0xa0
	s_cselect_b32 s0, 0x600, 0
	s_add_i32 s33, s0, s92
	s_cmpk_gt_i32 s33, 0x5ff
	s_mov_b32 s3, 0
	s_cbranch_scc1 .LBB0_1796
	s_mov_b32 s6, s33
	s_mov_b32 s7, s50
	s_movk_i32 s8, 0x600
	v_readlane_b32 s9, v235, 52
	v_readlane_b32 s2, v235, 9
	v_readlane_b32 s3, v235, 10
	v_readlane_b32 s4, v235, 19
	v_readlane_b32 s5, v235, 20
	s_mov_b32 s72, 0x3e38aa3b
	s_mov_b32 s73, 0x3e38aa3b
	v_lshrrev_b32_e32 v2, 3, v0
	v_and_b32_e32 v3, 7, v0
	v_lshlrev_b32_e32 v3, 4, v3
	s_movk_i32 s39, 0x90
	v_mad_u32_u24 v1, v2, s39, v3
	v_and_b32_e32 v5, 0xff, v0
	v_lshrrev_b32_e32 v6, 8, v0
	s_movk_i32 s39, 0x1180
	v_mul_u32_u24_e32 v4, s39, v6
	v_lshl_add_u32 v4, v5, 1, v4
	v_add_u32_e32 v4, 0xe100, v4
	v_lshlrev_b32_e32 v6, 4, v6
	v_lshlrev_b32_e32 v8, 2, v5
	v_add_u32_e32 v8, 0x16d00, v8
	v_subrev_u32_e32 v165, 16, v0
	s_movk_i32 s39, 0x81
	v_cmp_gt_u32_e64 s[42:43], s39, v165
	s_movk_i32 s39, 0xa0
	v_cmp_gt_u32_e64 s[48:49], s39, v0
	v_cmp_gt_u32_e64 s[46:47], 64, v0
	v_cmp_gt_u32_e64 s[44:45], 16, v146
	v_subrev_u32_e32 v165, 0x50, v0
	v_cmp_lt_i32_e32 vcc, 0, v165
	v_mov_b32_e32 v7, 0
	s_nop 0
	v_cndmask_b32_e64 v166, 0, 16, vcc
	v_lshlrev_b32_e32 v167, 0, v165
	v_sub_u32_e32 v168, 0, v167
	v_max_i32_e32 v167, v167, v168
	v_cvt_f32_u32_e32 v168, v167
	v_mul_f32_e32 v168, 0x3e000000, v168
	v_max_f32_e32 v168, 1.0, v168
	v_log_f32_e32 v168, v168
	v_cmp_gt_u32_e32 vcc, 8, v167
	v_mul_f32_e32 v168, 0x3f924925, v168
	v_cvt_i32_f32_e32 v168, v168
	v_min_i32_e32 v168, 7, v168
	v_add_u32_e32 v168, 8, v168
	v_cndmask_b32_e32 v168, v168, v167, vcc
	v_add_u32_e32 v168, v168, v166
	v_lshl_or_b32 v7, v168, 0, v7
	v_lshlrev_b32_e32 v167, 2, v165
	v_sub_u32_e32 v168, 0, v167
	v_max_i32_e32 v167, v167, v168
	v_cvt_f32_u32_e32 v168, v167
	v_mul_f32_e32 v168, 0x3e000000, v168
	v_max_f32_e32 v168, 1.0, v168
	v_log_f32_e32 v168, v168
	v_cmp_gt_u32_e32 vcc, 8, v167
	v_mul_f32_e32 v168, 0x3f924925, v168
	v_cvt_i32_f32_e32 v168, v168
	v_min_i32_e32 v168, 7, v168
	v_add_u32_e32 v168, 8, v168
	v_cndmask_b32_e32 v168, v168, v167, vcc
	v_add_u32_e32 v168, v168, v166
	v_lshl_or_b32 v7, v168, 8, v7
	v_lshlrev_b32_e32 v167, 4, v165
	v_sub_u32_e32 v168, 0, v167
	v_max_i32_e32 v167, v167, v168
	v_cvt_f32_u32_e32 v168, v167
	v_mul_f32_e32 v168, 0x3e000000, v168
	v_max_f32_e32 v168, 1.0, v168
	v_log_f32_e32 v168, v168
	v_cmp_gt_u32_e32 vcc, 8, v167
	v_mul_f32_e32 v168, 0x3f924925, v168
	v_cvt_i32_f32_e32 v168, v168
	v_min_i32_e32 v168, 7, v168
	v_add_u32_e32 v168, 8, v168
	v_cndmask_b32_e32 v168, v168, v167, vcc
	v_add_u32_e32 v168, v168, v166
	v_lshl_or_b32 v7, v168, 16, v7
	v_and_b32_e32 v165, 15, v146
	v_lshrrev_b32_e32 v166, 4, v146
	s_lshl_b32 s39, s9, 4
	v_add_u32_e32 v40, s39, v165
	s_movk_i32 s40, 0x90
	v_mul_u32_u24_e32 v34, s40, v40
	v_lshl_add_u32 v34, v166, 4, v34
	v_lshlrev_b32_e32 v167, 2, v166
	v_sub_u32_e32 v35, v167, v165
	v_lshlrev_b32_e32 v35, 2, v35
	v_add_u32_e32 v35, 0x16d40, v35
	v_add_u32_e32 v167, s39, v167
	v_lshlrev_b32_e32 v36, 2, v167
	v_add_u32_e32 v36, 0x16f80, v36
	s_movk_i32 s40, 0x230
	v_mul_u32_u24_e32 v37, s40, v165
	v_lshl_add_u32 v37, v167, 1, v37
	v_add_u32_e32 v37, 0xe100, v37
	v_add_u32_e32 v9, 0x2300, v37
	v_add_u32_e32 v118, 0x4600, v37
	v_add_u32_e32 v144, 0x6900, v37
	v_xor_b32_e32 v38, 16, v146
	v_lshlrev_b32_e32 v38, 2, v38
	v_xor_b32_e32 v39, 32, v146
	v_lshlrev_b32_e32 v39, 2, v39
	v_lshlrev_b32_e32 v41, 3, v166
	v_mov_b32_e32 v232, 0
	v_mov_b32_e32 v233, 0
	s_movk_i32 s40, 0x230
	v_mul_u32_u24_e32 v168, s40, v0
	v_add_u32_e32 v168, 0xe300, v168
	s_and_saveexec_b64 s[40:41], s[46:47]
	ds_write_b64 v168, v[232:233] offset:0
	ds_write_b64 v168, v[232:233] offset:8
	ds_write_b64 v168, v[232:233] offset:16
	ds_write_b64 v168, v[232:233] offset:24
	s_mov_b64 exec, s[40:41]
	s_and_b32 s39, s6, 15
	s_bfe_u32 s40, s6, 0x20004
	s_bfe_u32 s41, s6, 0x30006
	s_lshr_b32 s74, s6, 9
	s_lshl_b32 s75, s74, 1
	s_lshl_b32 s16, 1536, s75
	s_add_i32 s20, s75, 9
	s_add_i32 s26, s75, 4
	s_lshl_b32 s28, s74, 3
	s_lshr_b32 s29, 0x800, s75
	s_add_i32 s17, s29, -1
	s_sub_i32 s76, 4, s75
	s_lshr_b32 s77, s39, s76
	s_lshr_b32 s78, 16, s75
	s_add_i32 s78, s78, -1
	s_and_b32 s78, s39, s78
	s_lshl_b32 s19, s78, 7
	s_add_i32 s18, s19, 0xffffffc0
	s_lshl_b32 s79, s41, 11
	s_add_i32 s79, s79, s77
	s_lshl_b32 s80, s40, 7
	s_lshl_b32 s27, s40, 2
	s_mul_i32 s81, s79, 1536
	s_add_u32 s81, s81, s80
	s_add_u32 s81, s81, 0x28600000
	s_add_u32 s10, s2, s81
	s_addc_u32 s11, s3, 0
	s_lshl_b32 s82, s74, 14
	s_add_i32 s82, s82, s79
	s_lshl_b32 s83, s82, 9
	s_add_u32 s83, s83, s80
	s_add_u32 s83, s83, 0x34a00000
	s_add_u32 s12, s2, s83
	s_addc_u32 s13, s3, 0
	s_lshl_b32 s84, s82, 4
	s_add_u32 s84, s84, s27
	s_add_u32 s84, s84, 0x36200000
	s_add_u32 s14, s2, s84
	s_addc_u32 s15, s3, 0
	v_add_u32_e32 v165, s19, v2
	v_mad_u32_u24 v165, v165, s16, v3
	s_lshl_b32 s85, s16, 6
	global_load_dwordx4 v[120:123], v165, s[10:11] nt
	v_add_u32_e32 v166, s85, v165
	global_load_dwordx4 v[124:127], v166, s[10:11] nt
	v_add_u32_e32 v167, s18, v2
	v_med3_i32 v168, v167, 0, s17
	v_mad_u32_u24 v168, v168, s16, v3
	global_load_dwordx4 v[128:131], v168, s[10:11] offset:512
	v_add_u32_e32 v168, 64, v167
	v_med3_i32 v168, v168, 0, s17
	v_mad_u32_u24 v168, v168, s16, v3
	global_load_dwordx4 v[132:135], v168, s[10:11] offset:512
	v_add_u32_e32 v168, 0x80, v167
	v_med3_i32 v168, v168, 0, s17
	v_mad_u32_u24 v168, v168, s16, v3
	global_load_dwordx4 v[136:139], v168, s[10:11] offset:512
	v_add_u32_e32 v168, 0xc0, v167
	v_med3_i32 v168, v168, 0, s17
	v_mad_u32_u24 v168, v168, s16, v3
	global_load_dwordx4 v[140:143], v168, s[10:11] offset:512
	v_add_u32_e32 v169, s18, v5
	v_med3_i32 v169, v169, 0, s17
	v_mad_u32_u24 v169, v169, s16, v6
	global_load_dwordx4 v[148:151], v169, s[10:11] offset:1024
	global_load_dwordx4 v[152:155], v169, s[10:11] offset:1056
	global_load_dwordx4 v[156:159], v169, s[10:11] offset:1088
	global_load_dwordx4 v[160:163], v169, s[10:11] offset:1120
	v_bfe_u32 v171, v7, s28, 8
	v_lshl_add_u32 v171, v171, 4, s27
	s_mov_b64 exec, s[42:43]
	global_load_dword v164, v171, s[4:5]
	s_mov_b64 exec, -1

; DI void phase_final(const Args& A, int gw, int ngw, int lane) {
;     const bf16* xin = (const bf16*)(A.ws + WS_X1);
;     f32x4 gg[4];
; #pragma unroll
;     for (int j = 0; j < 4; ++j) gg[j] = ((const f32x4*)A.in[I_FG] + lane)[64 * j];
;     for (int tok = gw; tok < NT; tok += 2 * ngw) {
;         const int tokb = tok + ngw; const bool hb2 = tokb < NT;
;         f32x4 va[4], vb[4]; load_row_bf(xin + (size_t)tok * DM, lane, va); load_row_bf(xin + (size_t)(hb2 ? tokb : tok) * DM, lane, vb);
;         add_slots(A, tok, lane, va); add_slots(A, hb2 ? tokb : tok, lane, vb);
.LBB0_2948:
	s_cmp_gt_i32 s6, 21
	s_cselect_b64 s[2:3], -1, 0
	s_xor_b64 s[0:1], s[0:1], -1
	s_or_b64 s[0:1], s[2:3], s[0:1]
	s_and_b64 vcc, exec, s[0:1]
	s_cbranch_vccnz .LBB0_2997
	v_readlane_b32 s0, v234, 42
	v_readlane_b32 s1, v234, 43
	s_andn2_b64 vcc, exec, s[0:1]
	s_cbranch_vccnz .LBB0_2997
	s_cmpk_lg_i32 s50, 0x100
	s_cbranch_scc1 .Lrw2_orig
	s_waitcnt vmcnt(0) lgkmcnt(0)
	v_readlane_b32 s0, v235, 9
	v_readlane_b32 s1, v235, 10
	v_readlane_b32 s18, v235, 54
	v_readlane_b32 s20, v235, 4
	v_readlane_b32 s21, v235, 5
	v_readlane_b32 s14, v235, 6
	v_readlane_b32 s15, v235, 7
	v_lshlrev_b32_e32 v1, 3, v146
	v_lshlrev_b32_e32 v2, 2, v146
	v_lshlrev_b32_e32 v3, 4, v146
	v_xor_b32_e32 v4, 1, v146
	v_lshlrev_b32_e32 v4, 2, v4
	v_xor_b32_e32 v5, 2, v146
	v_lshlrev_b32_e32 v5, 2, v5
	v_xor_b32_e32 v6, 4, v146
	v_lshlrev_b32_e32 v6, 2, v6
	v_xor_b32_e32 v7, 8, v146
	v_lshlrev_b32_e32 v7, 2, v7
	v_xor_b32_e32 v8, 16, v146
	v_lshlrev_b32_e32 v8, 2, v8
	v_xor_b32_e32 v9, 32, v146
	v_lshlrev_b32_e32 v9, 2, v9
	v_mov_b32_e32 v171, 0x358637bd
	s_mov_b32 s39, 0x3a800000
	s_mov_b32 s40, 0x800000
	s_lshl_b32 s19, s18, 11
	s_add_u32 s4, s0, 0x22600000
	s_addc_u32 s5, s1, 0
	s_add_u32 s4, s4, s19
	s_addc_u32 s5, s5, 0
	s_lshl_b32 s34, s18, 6
	s_add_u32 s6, s0, 0x2c700000
	s_addc_u32 s7, s1, 0
	s_add_u32 s6, s6, s34
	s_addc_u32 s7, s7, 0
	s_add_u32 s12, s0, 0x3ba00000
	s_addc_u32 s13, s1, 0
	s_lshl_b32 s34, s18, 12
	s_add_u32 s14, s14, s34
	s_addc_u32 s15, s15, 0
	v_mov_b32_e32 v10, -1
	v_mov_b32_e32 v11, -1
	v_mov_b32_e32 v12, -1
	v_mov_b32_e32 v13, -1
	v_mov_b32_e32 v14, -1
	v_mov_b32_e32 v15, -1
	v_mov_b32_e32 v16, -1
	v_mov_b32_e32 v17, -1
	s_mov_b64 exec, 0xffff
	s_mov_b64 s[34:35], s[6:7]
	global_load_dword v10, v2, s[34:35] nt
	s_add_u32 s34, s6, 0x20000
	s_addc_u32 s35, s7, 0
	global_load_dword v11, v2, s[34:35] nt
	s_add_u32 s34, s6, 0x40000
	s_addc_u32 s35, s7, 0
	global_load_dword v12, v2, s[34:35] nt
	s_add_u32 s34, s6, 0x60000
	s_addc_u32 s35, s7, 0
	global_load_dword v13, v2, s[34:35] nt
	s_add_u32 s34, s6, 0x80000
	s_addc_u32 s35, s7, 0
	global_load_dword v14, v2, s[34:35] nt
	s_add_u32 s34, s6, 0xa0000
	s_addc_u32 s35, s7, 0
	global_load_dword v15, v2, s[34:35] nt
	s_add_u32 s34, s6, 0xc0000
	s_addc_u32 s35, s7, 0
	global_load_dword v16, v2, s[34:35] nt
	s_add_u32 s34, s6, 0xe0000
	s_addc_u32 s35, s7, 0
	global_load_dword v17, v2, s[34:35] nt
	s_mov_b64 exec, -1
	s_mov_b64 s[34:35], s[4:5]
	global_load_dwordx2 v[34:35], v1, s[34:35] nt
	global_load_dwordx2 v[36:37], v1, s[34:35] offset:512 nt
	global_load_dwordx2 v[38:39], v1, s[34:35] offset:1024 nt
	global_load_dwordx2 v[40:41], v1, s[34:35] offset:1536 nt
	s_add_u32 s34, s4, 0x400000
	s_addc_u32 s35, s5, 0
	global_load_dwordx2 v[42:43], v1, s[34:35] nt
	global_load_dwordx2 v[44:45], v1, s[34:35] offset:512 nt
	global_load_dwordx2 v[46:47], v1, s[34:35] offset:1024 nt
	global_load_dwordx2 v[48:49], v1, s[34:35] offset:1536 nt
	s_add_u32 s34, s4, 0x800000
	s_addc_u32 s35, s5, 0
	global_load_dwordx2 v[50:51], v1, s[34:35] nt
	global_load_dwordx2 v[52:53], v1, s[34:35] offset:512 nt
	global_load_dwordx2 v[54:55], v1, s[34:35] offset:1024 nt
	global_load_dwordx2 v[56:57], v1, s[34:35] offset:1536 nt
	s_add_u32 s34, s4, 0xc00000
	s_addc_u32 s35, s5, 0
	global_load_dwordx2 v[58:59], v1, s[34:35] nt
	global_load_dwordx2 v[60:61], v1, s[34:35] offset:512 nt
	global_load_dwordx2 v[62:63], v1, s[34:35] offset:1024 nt
	global_load_dwordx2 v[64:65], v1, s[34:35] offset:1536 nt
	s_add_u32 s34, s4, 0x1000000
	s_addc_u32 s35, s5, 0
	global_load_dwordx2 v[66:67], v1, s[34:35] nt
	global_load_dwordx2 v[68:69], v1, s[34:35] offset:512 nt
	global_load_dwordx2 v[70:71], v1, s[34:35] offset:1024 nt
	global_load_dwordx2 v[72:73], v1, s[34:35] offset:1536 nt
	s_add_u32 s34, s4, 0x1400000
	s_addc_u32 s35, s5, 0
	global_load_dwordx2 v[74:75], v1, s[34:35] nt
	global_load_dwordx2 v[76:77], v1, s[34:35] offset:512 nt
	global_load_dwordx2 v[78:79], v1, s[34:35] offset:1024 nt
	global_load_dwordx2 v[80:81], v1, s[34:35] offset:1536 nt
	s_add_u32 s34, s4, 0x1800000
	s_addc_u32 s35, s5, 0
	global_load_dwordx2 v[82:83], v1, s[34:35] nt
	global_load_dwordx2 v[84:85], v1, s[34:35] offset:512 nt
	global_load_dwordx2 v[86:87], v1, s[34:35] offset:1024 nt
	global_load_dwordx2 v[88:89], v1, s[34:35] offset:1536 nt
	s_add_u32 s34, s4, 0x1c00000
	s_addc_u32 s35, s5, 0
	global_load_dwordx2 v[90:91], v1, s[34:35] nt
	global_load_dwordx2 v[92:93], v1, s[34:35] offset:512 nt
	global_load_dwordx2 v[94:95], v1, s[34:35] offset:1024 nt
	global_load_dwordx2 v[96:97], v1, s[34:35] offset:1536 nt
	global_load_dwordx4 v[18:21], v3, s[20:21]
	global_load_dwordx4 v[22:25], v3, s[20:21] offset:1024
	global_load_dwordx4 v[26:29], v3, s[20:21] offset:2048
	global_load_dwordx4 v[30:33], v3, s[20:21] offset:3072
	s_waitcnt vmcnt(36)
	v_cmp_le_i32_e64 s[66:67], 0, v10
	v_cmp_le_i32_e64 s[68:69], 0, v11
	v_cmp_le_i32_e64 s[70:71], 0, v12
	v_cmp_le_i32_e64 s[72:73], 0, v13
	v_cmp_le_i32_e64 s[74:75], 0, v14
	v_cmp_le_i32_e64 s[76:77], 0, v15
	v_cmp_le_i32_e64 s[78:79], 0, v16
	v_cmp_le_i32_e64 s[80:81], 0, v17
	s_nop 1
	s_mov_b32 s38, 1

; DI float wave_sum(float v) { v = row16_sum(v); v += __shfl_xor(v, 16); v += __shfl_xor(v, 32); return v; }
; DI float row_rstd(const f32x4 (&v)[4]) {
;     float s = 0.f;
; #pragma unroll
;     for (int j = 0; j < 4; ++j) s += (v[j][0] * v[j][0] + v[j][1] * v[j][1]) + (v[j][2] * v[j][2] + v[j][3] * v[j][3]);
;     return rsqrtf(wave_sum(s) * (1.f / DM) + RMS_EPS);
.Lrw2_a0_7:
	s_or_b32 s34, s66, s68
	s_or_b32 s34, s34, s70
	s_or_b32 s34, s34, s72
	s_cmp_lg_u32 s34, 0
	s_cbranch_scc1 .Lrw2_round0
	v_mul_f32_e32 v128, v172, v172
	v_mul_f32_e32 v129, v174, v174
	v_fmac_f32_e32 v128, v173, v173
	v_fmac_f32_e32 v129, v175, v175
	v_add_f32_e32 v128, v128, v129
	v_mul_f32_e32 v132, v188, v188
	v_mul_f32_e32 v133, v190, v190
	v_fmac_f32_e32 v132, v189, v189
	v_fmac_f32_e32 v133, v191, v191
	v_add_f32_e32 v132, v132, v133
	v_mul_f32_e32 v136, v204, v204
	v_mul_f32_e32 v137, v206, v206
	v_fmac_f32_e32 v136, v205, v205
	v_fmac_f32_e32 v137, v207, v207
	v_add_f32_e32 v136, v136, v137
	v_mul_f32_e32 v252, v236, v236
	v_mul_f32_e32 v253, v238, v238
	v_fmac_f32_e32 v252, v237, v237
	v_fmac_f32_e32 v253, v239, v239
	v_add_f32_e32 v252, v252, v253
	v_mul_f32_e32 v129, v176, v176
	v_mul_f32_e32 v254, v178, v178
	v_fmac_f32_e32 v129, v177, v177
	v_fmac_f32_e32 v254, v179, v179
	v_add_f32_e32 v129, v129, v254
	v_add_f32_e32 v128, v128, v129
	v_mul_f32_e32 v133, v192, v192
	v_mul_f32_e32 v255, v194, v194
	v_fmac_f32_e32 v133, v193, v193
	v_fmac_f32_e32 v255, v195, v195
	v_add_f32_e32 v133, v133, v255
	v_add_f32_e32 v132, v132, v133
	v_mul_f32_e32 v137, v208, v208
	v_mul_f32_e32 v254, v210, v210
	v_fmac_f32_e32 v137, v209, v209
	v_fmac_f32_e32 v254, v211, v211
	v_add_f32_e32 v137, v137, v254
	v_add_f32_e32 v136, v136, v137
	v_mul_f32_e32 v253, v240, v240
	v_mul_f32_e32 v255, v242, v242
	v_fmac_f32_e32 v253, v241, v241
	v_fmac_f32_e32 v255, v243, v243
	v_add_f32_e32 v253, v253, v255
	v_add_f32_e32 v252, v252, v253
	v_mul_f32_e32 v129, v180, v180
	v_mul_f32_e32 v254, v182, v182
	v_fmac_f32_e32 v129, v181, v181
	v_fmac_f32_e32 v254, v183, v183
	v_add_f32_e32 v129, v129, v254
	v_add_f32_e32 v128, v128, v129
	v_mul_f32_e32 v133, v196, v196
	v_mul_f32_e32 v255, v198, v198
	v_fmac_f32_e32 v133, v197, v197
	v_fmac_f32_e32 v255, v199, v199
	v_add_f32_e32 v133, v133, v255
	v_add_f32_e32 v132, v132, v133
	v_mul_f32_e32 v137, v212, v212
	v_mul_f32_e32 v254, v214, v214
	v_fmac_f32_e32 v137, v213, v213
	v_fmac_f32_e32 v254, v215, v215
	v_add_f32_e32 v137, v137, v254
	v_add_f32_e32 v136, v136, v137
	v_mul_f32_e32 v253, v244, v244
	v_mul_f32_e32 v255, v246, v246
	v_fmac_f32_e32 v253, v245, v245
	v_fmac_f32_e32 v255, v247, v247
	v_add_f32_e32 v253, v253, v255
	v_add_f32_e32 v252, v252, v253
	v_mul_f32_e32 v129, v184, v184
	v_mul_f32_e32 v254, v186, v186
	v_fmac_f32_e32 v129, v185, v185
	v_fmac_f32_e32 v254, v187, v187
	v_add_f32_e32 v129, v129, v254
	v_add_f32_e32 v128, v128, v129
	v_mul_f32_e32 v133, v200, v200
	v_mul_f32_e32 v255, v202, v202
	v_fmac_f32_e32 v133, v201, v201
	v_fmac_f32_e32 v255, v203, v203
	v_add_f32_e32 v133, v133, v255
	v_add_f32_e32 v132, v132, v133
	v_mul_f32_e32 v137, v216, v216
	v_mul_f32_e32 v254, v218, v218
	v_fmac_f32_e32 v137, v217, v217
	v_fmac_f32_e32 v254, v219, v219
	v_add_f32_e32 v137, v137, v254
	v_add_f32_e32 v136, v136, v137
	v_mul_f32_e32 v253, v248, v248
	v_mul_f32_e32 v255, v250, v250
	v_fmac_f32_e32 v253, v249, v249
	v_fmac_f32_e32 v255, v251, v251
	v_add_f32_e32 v253, v253, v255
	v_add_f32_e32 v252, v252, v253
	s_nop 0
	ds_bpermute_b32 v129, v4, v128
	ds_bpermute_b32 v133, v4, v132
	ds_bpermute_b32 v137, v4, v136
	ds_bpermute_b32 v253, v4, v252
	s_waitcnt lgkmcnt(0)
	v_add_f32_e32 v128, v128, v129
	v_add_f32_e32 v132, v132, v133
	v_add_f32_e32 v136, v136, v137
	v_add_f32_e32 v252, v252, v253
	s_nop 0
	ds_bpermute_b32 v129, v5, v128
	ds_bpermute_b32 v133, v5, v132
	ds_bpermute_b32 v137, v5, v136
	ds_bpermute_b32 v253, v5, v252
	s_waitcnt lgkmcnt(0)
	v_add_f32_e32 v128, v128, v129
	v_add_f32_e32 v132, v132, v133
	v_add_f32_e32 v136, v136, v137
	v_add_f32_e32 v252, v252, v253
	s_nop 0
	ds_bpermute_b32 v129, v6, v128
	ds_bpermute_b32 v133, v6, v132
	ds_bpermute_b32 v137, v6, v136
	ds_bpermute_b32 v253, v6, v252
	s_waitcnt lgkmcnt(0)
	v_add_f32_e32 v128, v128, v129
	v_add_f32_e32 v132, v132, v133
	v_add_f32_e32 v136, v136, v137
	v_add_f32_e32 v252, v252, v253
	s_nop 0
	ds_bpermute_b32 v129, v7, v128
	ds_bpermute_b32 v133, v7, v132
	ds_bpermute_b32 v137, v7, v136
	ds_bpermute_b32 v253, v7, v252
	s_waitcnt lgkmcnt(0)
	v_add_f32_e32 v128, v128, v129
	v_add_f32_e32 v132, v132, v133
	v_add_f32_e32 v136, v136, v137
	v_add_f32_e32 v252, v252, v253
	s_nop 0
	ds_bpermute_b32 v129, v8, v128
	ds_bpermute_b32 v133, v8, v132
	ds_bpermute_b32 v137, v8, v136
	ds_bpermute_b32 v253, v8, v252
	s_waitcnt lgkmcnt(0)
	v_add_f32_e32 v128, v128, v129
	v_add_f32_e32 v132, v132, v133
	v_add_f32_e32 v136, v136, v137
	v_add_f32_e32 v252, v252, v253
	s_nop 0
	ds_bpermute_b32 v129, v9, v128
	ds_bpermute_b32 v133, v9, v132
	ds_bpermute_b32 v137, v9, v136
	ds_bpermute_b32 v253, v9, v252
	s_waitcnt lgkmcnt(0)
; DI void phase_final(const Args& A, int gw, int ngw, int lane) {
;     const bf16* xin = (const bf16*)(A.ws + WS_X1);
;     f32x4 gg[4];
; #pragma unroll
;     for (int j = 0; j < 4; ++j) gg[j] = ((const f32x4*)A.in[I_FG] + lane)[64 * j];
;     for (int tok = gw; tok < NT; tok += 2 * ngw) {
;         const int tokb = tok + ngw; const bool hb2 = tokb < NT;
;         f32x4 va[4], vb[4]; load_row_bf(xin + (size_t)tok * DM, lane, va); load_row_bf(xin + (size_t)(hb2 ? tokb : tok) * DM, lane, vb);
;         add_slots(A, tok, lane, va); add_slots(A, hb2 ? tokb : tok, lane, vb);
;         const float ra = row_rstd(va), rb = row_rstd(vb); f32x4* oa = (f32x4*)(A.out + (size_t)tok * DM) + lane; f32x4* ob = (f32x4*)(A.out + (size_t)tokb * DM) + lane;
; #pragma unroll
;         for (int j = 0; j < 4; ++j) { oa[64 * j] = va[j] * ra * gg[j]; if (hb2) ob[64 * j] = vb[j] * rb * gg[j]; }
;     }
	v_add_f32_e32 v128, v128, v129
	v_add_f32_e32 v132, v132, v133
	v_add_f32_e32 v136, v136, v137
	v_add_f32_e32 v252, v252, v253
	v_fma_f32 v128, v128, s39, v171
	v_mul_f32_e32 v129, 0x4b800000, v128
	v_cmp_gt_f32_e32 vcc, s40, v128
	s_nop 1
	v_cndmask_b32_e32 v128, v128, v129, vcc
	v_rsq_f32_e32 v128, v128
	s_nop 0
	v_mul_f32_e32 v129, 0x45800000, v128
	v_cndmask_b32_e32 v128, v128, v129, vcc
	v_fma_f32 v132, v132, s39, v171
	v_mul_f32_e32 v133, 0x4b800000, v132
	v_cmp_gt_f32_e32 vcc, s40, v132
	s_nop 1
	v_cndmask_b32_e32 v132, v132, v133, vcc
	v_rsq_f32_e32 v132, v132
	s_nop 0
	v_mul_f32_e32 v133, 0x45800000, v132
	v_cndmask_b32_e32 v132, v132, v133, vcc
	v_fma_f32 v136, v136, s39, v171
	v_mul_f32_e32 v137, 0x4b800000, v136
	v_cmp_gt_f32_e32 vcc, s40, v136
	s_nop 1
	v_cndmask_b32_e32 v136, v136, v137, vcc
	v_rsq_f32_e32 v136, v136
	s_nop 0
	v_mul_f32_e32 v137, 0x45800000, v136
	v_cndmask_b32_e32 v136, v136, v137, vcc
	v_fma_f32 v252, v252, s39, v171
	v_mul_f32_e32 v253, 0x4b800000, v252
	v_cmp_gt_f32_e32 vcc, s40, v252
	s_nop 1
	v_cndmask_b32_e32 v252, v252, v253, vcc
	v_rsq_f32_e32 v252, v252
	s_nop 0
	v_mul_f32_e32 v253, 0x45800000, v252
	v_cndmask_b32_e32 v252, v252, v253, vcc
	v_pk_mul_f32 v[172:173], v[172:173], v[128:129] op_sel_hi:[1,0]
	v_pk_mul_f32 v[174:175], v[174:175], v[128:129] op_sel_hi:[1,0]
	v_pk_mul_f32 v[176:177], v[176:177], v[128:129] op_sel_hi:[1,0]
	v_pk_mul_f32 v[178:179], v[178:179], v[128:129] op_sel_hi:[1,0]
	v_pk_mul_f32 v[180:181], v[180:181], v[128:129] op_sel_hi:[1,0]
	v_pk_mul_f32 v[182:183], v[182:183], v[128:129] op_sel_hi:[1,0]
	v_pk_mul_f32 v[184:185], v[184:185], v[128:129] op_sel_hi:[1,0]
	v_pk_mul_f32 v[186:187], v[186:187], v[128:129] op_sel_hi:[1,0]
	v_pk_mul_f32 v[172:173], v[172:173], v[18:19]
	v_pk_mul_f32 v[174:175], v[174:175], v[20:21]
	v_pk_mul_f32 v[176:177], v[176:177], v[22:23]
	v_pk_mul_f32 v[178:179], v[178:179], v[24:25]
	v_pk_mul_f32 v[180:181], v[180:181], v[26:27]
	v_pk_mul_f32 v[182:183], v[182:183], v[28:29]
	v_pk_mul_f32 v[184:185], v[184:185], v[30:31]
	v_pk_mul_f32 v[186:187], v[186:187], v[32:33]
	s_mov_b64 s[34:35], s[14:15]
	global_store_dwordx4 v3, v[172:175], s[34:35] nt
	global_store_dwordx4 v3, v[176:179], s[34:35] offset:1024 nt
	global_store_dwordx4 v3, v[180:183], s[34:35] offset:2048 nt
	global_store_dwordx4 v3, v[184:187], s[34:35] offset:3072 nt
	v_pk_mul_f32 v[188:189], v[188:189], v[132:133] op_sel_hi:[1,0]
	v_pk_mul_f32 v[190:191], v[190:191], v[132:133] op_sel_hi:[1,0]
	v_pk_mul_f32 v[192:193], v[192:193], v[132:133] op_sel_hi:[1,0]
	v_pk_mul_f32 v[194:195], v[194:195], v[132:133] op_sel_hi:[1,0]
	v_pk_mul_f32 v[196:197], v[196:197], v[132:133] op_sel_hi:[1,0]
	v_pk_mul_f32 v[198:199], v[198:199], v[132:133] op_sel_hi:[1,0]
	v_pk_mul_f32 v[200:201], v[200:201], v[132:133] op_sel_hi:[1,0]
	v_pk_mul_f32 v[202:203], v[202:203], v[132:133] op_sel_hi:[1,0]
	v_pk_mul_f32 v[188:189], v[188:189], v[18:19]
	v_pk_mul_f32 v[190:191], v[190:191], v[20:21]
	v_pk_mul_f32 v[192:193], v[192:193], v[22:23]
	v_pk_mul_f32 v[194:195], v[194:195], v[24:25]
	v_pk_mul_f32 v[196:197], v[196:197], v[26:27]
	v_pk_mul_f32 v[198:199], v[198:199], v[28:29]
	v_pk_mul_f32 v[200:201], v[200:201], v[30:31]
	v_pk_mul_f32 v[202:203], v[202:203], v[32:33]
	s_add_u32 s34, s14, 0x800000
	s_addc_u32 s35, s15, 0
	global_store_dwordx4 v3, v[188:191], s[34:35] nt
	global_store_dwordx4 v3, v[192:195], s[34:35] offset:1024 nt
	global_store_dwordx4 v3, v[196:199], s[34:35] offset:2048 nt
	global_store_dwordx4 v3, v[200:203], s[34:35] offset:3072 nt
	v_pk_mul_f32 v[204:205], v[204:205], v[136:137] op_sel_hi:[1,0]
	v_pk_mul_f32 v[206:207], v[206:207], v[136:137] op_sel_hi:[1,0]
	v_pk_mul_f32 v[208:209], v[208:209], v[136:137] op_sel_hi:[1,0]
	v_pk_mul_f32 v[210:211], v[210:211], v[136:137] op_sel_hi:[1,0]
	v_pk_mul_f32 v[212:213], v[212:213], v[136:137] op_sel_hi:[1,0]
	v_pk_mul_f32 v[214:215], v[214:215], v[136:137] op_sel_hi:[1,0]
	v_pk_mul_f32 v[216:217], v[216:217], v[136:137] op_sel_hi:[1,0]
	v_pk_mul_f32 v[218:219], v[218:219], v[136:137] op_sel_hi:[1,0]
	v_pk_mul_f32 v[204:205], v[204:205], v[18:19]
	v_pk_mul_f32 v[206:207], v[206:207], v[20:21]
	v_pk_mul_f32 v[208:209], v[208:209], v[22:23]
	v_pk_mul_f32 v[210:211], v[210:211], v[24:25]
	v_pk_mul_f32 v[212:213], v[212:213], v[26:27]
	v_pk_mul_f32 v[214:215], v[214:215], v[28:29]
	v_pk_mul_f32 v[216:217], v[216:217], v[30:31]
	v_pk_mul_f32 v[218:219], v[218:219], v[32:33]
	s_add_u32 s34, s14, 0x1000000
	s_addc_u32 s35, s15, 0
	global_store_dwordx4 v3, v[204:207], s[34:35] nt
	global_store_dwordx4 v3, v[208:211], s[34:35] offset:1024 nt
	global_store_dwordx4 v3, v[212:215], s[34:35] offset:2048 nt
	global_store_dwordx4 v3, v[216:219], s[34:35] offset:3072 nt
	v_pk_mul_f32 v[236:237], v[236:237], v[252:253] op_sel_hi:[1,0]
	v_pk_mul_f32 v[238:239], v[238:239], v[252:253] op_sel_hi:[1,0]
	v_pk_mul_f32 v[240:241], v[240:241], v[252:253] op_sel_hi:[1,0]
	v_pk_mul_f32 v[242:243], v[242:243], v[252:253] op_sel_hi:[1,0]
	v_pk_mul_f32 v[244:245], v[244:245], v[252:253] op_sel_hi:[1,0]
	v_pk_mul_f32 v[246:247], v[246:247], v[252:253] op_sel_hi:[1,0]
	v_pk_mul_f32 v[248:249], v[248:249], v[252:253] op_sel_hi:[1,0]
	v_pk_mul_f32 v[250:251], v[250:251], v[252:253] op_sel_hi:[1,0]
	v_pk_mul_f32 v[236:237], v[236:237], v[18:19]
	v_pk_mul_f32 v[238:239], v[238:239], v[20:21]
	v_pk_mul_f32 v[240:241], v[240:241], v[22:23]
	v_pk_mul_f32 v[242:243], v[242:243], v[24:25]
	v_pk_mul_f32 v[244:245], v[244:245], v[26:27]
	v_pk_mul_f32 v[246:247], v[246:247], v[28:29]
	v_pk_mul_f32 v[248:249], v[248:249], v[30:31]
	v_pk_mul_f32 v[250:251], v[250:251], v[32:33]
	s_add_u32 s34, s14, 0x1800000
	s_addc_u32 s35, s15, 0
	global_store_dwordx4 v3, v[236:239], s[34:35] nt
	global_store_dwordx4 v3, v[240:243], s[34:35] offset:1024 nt
	global_store_dwordx4 v3, v[244:247], s[34:35] offset:2048 nt
	global_store_dwordx4 v3, v[248:251], s[34:35] offset:3072 nt
	s_mov_b32 s38, 1

; DI float wave_sum(float v) { v = row16_sum(v); v += __shfl_xor(v, 16); v += __shfl_xor(v, 32); return v; }
; DI float row_rstd(const f32x4 (&v)[4]) {
;     float s = 0.f;
; #pragma unroll
;     for (int j = 0; j < 4; ++j) s += (v[j][0] * v[j][0] + v[j][1] * v[j][1]) + (v[j][2] * v[j][2] + v[j][3] * v[j][3]);
;     return rsqrtf(wave_sum(s) * (1.f / DM) + RMS_EPS);
.Lrw2_a1_7:
	s_or_b32 s34, s74, s76
	s_or_b32 s34, s34, s78
	s_or_b32 s34, s34, s80
	s_cmp_lg_u32 s34, 0
	s_cbranch_scc1 .Lrw2_round1
	v_mul_f32_e32 v128, v172, v172
	v_mul_f32_e32 v129, v174, v174
	v_fmac_f32_e32 v128, v173, v173
	v_fmac_f32_e32 v129, v175, v175
	v_add_f32_e32 v128, v128, v129
	v_mul_f32_e32 v132, v188, v188
	v_mul_f32_e32 v133, v190, v190
	v_fmac_f32_e32 v132, v189, v189
	v_fmac_f32_e32 v133, v191, v191
	v_add_f32_e32 v132, v132, v133
	v_mul_f32_e32 v136, v204, v204
	v_mul_f32_e32 v137, v206, v206
	v_fmac_f32_e32 v136, v205, v205
	v_fmac_f32_e32 v137, v207, v207
	v_add_f32_e32 v136, v136, v137
	v_mul_f32_e32 v252, v236, v236
	v_mul_f32_e32 v253, v238, v238
	v_fmac_f32_e32 v252, v237, v237
	v_fmac_f32_e32 v253, v239, v239
	v_add_f32_e32 v252, v252, v253
	v_mul_f32_e32 v129, v176, v176
	v_mul_f32_e32 v254, v178, v178
	v_fmac_f32_e32 v129, v177, v177
	v_fmac_f32_e32 v254, v179, v179
	v_add_f32_e32 v129, v129, v254
	v_add_f32_e32 v128, v128, v129
	v_mul_f32_e32 v133, v192, v192
	v_mul_f32_e32 v255, v194, v194
	v_fmac_f32_e32 v133, v193, v193
	v_fmac_f32_e32 v255, v195, v195
	v_add_f32_e32 v133, v133, v255
	v_add_f32_e32 v132, v132, v133
	v_mul_f32_e32 v137, v208, v208
	v_mul_f32_e32 v254, v210, v210
	v_fmac_f32_e32 v137, v209, v209
	v_fmac_f32_e32 v254, v211, v211
	v_add_f32_e32 v137, v137, v254
	v_add_f32_e32 v136, v136, v137
	v_mul_f32_e32 v253, v240, v240
	v_mul_f32_e32 v255, v242, v242
	v_fmac_f32_e32 v253, v241, v241
	v_fmac_f32_e32 v255, v243, v243
	v_add_f32_e32 v253, v253, v255
	v_add_f32_e32 v252, v252, v253
	v_mul_f32_e32 v129, v180, v180
	v_mul_f32_e32 v254, v182, v182
	v_fmac_f32_e32 v129, v181, v181
	v_fmac_f32_e32 v254, v183, v183
	v_add_f32_e32 v129, v129, v254
	v_add_f32_e32 v128, v128, v129
	v_mul_f32_e32 v133, v196, v196
	v_mul_f32_e32 v255, v198, v198
	v_fmac_f32_e32 v133, v197, v197
	v_fmac_f32_e32 v255, v199, v199
	v_add_f32_e32 v133, v133, v255
	v_add_f32_e32 v132, v132, v133
	v_mul_f32_e32 v137, v212, v212
	v_mul_f32_e32 v254, v214, v214
	v_fmac_f32_e32 v137, v213, v213
	v_fmac_f32_e32 v254, v215, v215
	v_add_f32_e32 v137, v137, v254
	v_add_f32_e32 v136, v136, v137
	v_mul_f32_e32 v253, v244, v244
	v_mul_f32_e32 v255, v246, v246
	v_fmac_f32_e32 v253, v245, v245
	v_fmac_f32_e32 v255, v247, v247
	v_add_f32_e32 v253, v253, v255
	v_add_f32_e32 v252, v252, v253
	v_mul_f32_e32 v129, v184, v184
	v_mul_f32_e32 v254, v186, v186
	v_fmac_f32_e32 v129, v185, v185
	v_fmac_f32_e32 v254, v187, v187
	v_add_f32_e32 v129, v129, v254
	v_add_f32_e32 v128, v128, v129
	v_mul_f32_e32 v133, v200, v200
	v_mul_f32_e32 v255, v202, v202
	v_fmac_f32_e32 v133, v201, v201
	v_fmac_f32_e32 v255, v203, v203
	v_add_f32_e32 v133, v133, v255
	v_add_f32_e32 v132, v132, v133
	v_mul_f32_e32 v137, v216, v216
	v_mul_f32_e32 v254, v218, v218
	v_fmac_f32_e32 v137, v217, v217
	v_fmac_f32_e32 v254, v219, v219
	v_add_f32_e32 v137, v137, v254
	v_add_f32_e32 v136, v136, v137
	v_mul_f32_e32 v253, v248, v248
	v_mul_f32_e32 v255, v250, v250
	v_fmac_f32_e32 v253, v249, v249
	v_fmac_f32_e32 v255, v251, v251
	v_add_f32_e32 v253, v253, v255
	v_add_f32_e32 v252, v252, v253
	s_nop 0
	ds_bpermute_b32 v129, v4, v128
	ds_bpermute_b32 v133, v4, v132
	ds_bpermute_b32 v137, v4, v136
	ds_bpermute_b32 v253, v4, v252
	s_waitcnt lgkmcnt(0)
	v_add_f32_e32 v128, v128, v129
	v_add_f32_e32 v132, v132, v133
	v_add_f32_e32 v136, v136, v137
	v_add_f32_e32 v252, v252, v253
	s_nop 0
	ds_bpermute_b32 v129, v5, v128
	ds_bpermute_b32 v133, v5, v132
	ds_bpermute_b32 v137, v5, v136
	ds_bpermute_b32 v253, v5, v252
	s_waitcnt lgkmcnt(0)
	v_add_f32_e32 v128, v128, v129
	v_add_f32_e32 v132, v132, v133
	v_add_f32_e32 v136, v136, v137
	v_add_f32_e32 v252, v252, v253
	s_nop 0
	ds_bpermute_b32 v129, v6, v128
	ds_bpermute_b32 v133, v6, v132
	ds_bpermute_b32 v137, v6, v136
	ds_bpermute_b32 v253, v6, v252
	s_waitcnt lgkmcnt(0)
	v_add_f32_e32 v128, v128, v129
	v_add_f32_e32 v132, v132, v133
	v_add_f32_e32 v136, v136, v137
	v_add_f32_e32 v252, v252, v253
	s_nop 0
	ds_bpermute_b32 v129, v7, v128
	ds_bpermute_b32 v133, v7, v132
	ds_bpermute_b32 v137, v7, v136
	ds_bpermute_b32 v253, v7, v252
	s_waitcnt lgkmcnt(0)
	v_add_f32_e32 v128, v128, v129
	v_add_f32_e32 v132, v132, v133
	v_add_f32_e32 v136, v136, v137
	v_add_f32_e32 v252, v252, v253
	s_nop 0
	ds_bpermute_b32 v129, v8, v128
	ds_bpermute_b32 v133, v8, v132
	ds_bpermute_b32 v137, v8, v136
	ds_bpermute_b32 v253, v8, v252
	s_waitcnt lgkmcnt(0)
	v_add_f32_e32 v128, v128, v129
	v_add_f32_e32 v132, v132, v133
	v_add_f32_e32 v136, v136, v137
	v_add_f32_e32 v252, v252, v253
	s_nop 0
	ds_bpermute_b32 v129, v9, v128
	ds_bpermute_b32 v133, v9, v132
	ds_bpermute_b32 v137, v9, v136
	ds_bpermute_b32 v253, v9, v252
	s_waitcnt lgkmcnt(0)
; DI void phase_final(const Args& A, int gw, int ngw, int lane) {
;     const bf16* xin = (const bf16*)(A.ws + WS_X1);
;     f32x4 gg[4];
; #pragma unroll
;     for (int j = 0; j < 4; ++j) gg[j] = ((const f32x4*)A.in[I_FG] + lane)[64 * j];
;     for (int tok = gw; tok < NT; tok += 2 * ngw) {
;         const int tokb = tok + ngw; const bool hb2 = tokb < NT;
;         f32x4 va[4], vb[4]; load_row_bf(xin + (size_t)tok * DM, lane, va); load_row_bf(xin + (size_t)(hb2 ? tokb : tok) * DM, lane, vb);
;         add_slots(A, tok, lane, va); add_slots(A, hb2 ? tokb : tok, lane, vb);
;         const float ra = row_rstd(va), rb = row_rstd(vb); f32x4* oa = (f32x4*)(A.out + (size_t)tok * DM) + lane; f32x4* ob = (f32x4*)(A.out + (size_t)tokb * DM) + lane;
; #pragma unroll
;         for (int j = 0; j < 4; ++j) { oa[64 * j] = va[j] * ra * gg[j]; if (hb2) ob[64 * j] = vb[j] * rb * gg[j]; }
;     }
	v_add_f32_e32 v128, v128, v129
	v_add_f32_e32 v132, v132, v133
	v_add_f32_e32 v136, v136, v137
	v_add_f32_e32 v252, v252, v253
	v_fma_f32 v128, v128, s39, v171
	v_mul_f32_e32 v129, 0x4b800000, v128
	v_cmp_gt_f32_e32 vcc, s40, v128
	s_nop 1
	v_cndmask_b32_e32 v128, v128, v129, vcc
	v_rsq_f32_e32 v128, v128
	s_nop 0
	v_mul_f32_e32 v129, 0x45800000, v128
	v_cndmask_b32_e32 v128, v128, v129, vcc
	v_fma_f32 v132, v132, s39, v171
	v_mul_f32_e32 v133, 0x4b800000, v132
	v_cmp_gt_f32_e32 vcc, s40, v132
	s_nop 1
	v_cndmask_b32_e32 v132, v132, v133, vcc
	v_rsq_f32_e32 v132, v132
	s_nop 0
	v_mul_f32_e32 v133, 0x45800000, v132
	v_cndmask_b32_e32 v132, v132, v133, vcc
	v_fma_f32 v136, v136, s39, v171
	v_mul_f32_e32 v137, 0x4b800000, v136
	v_cmp_gt_f32_e32 vcc, s40, v136
	s_nop 1
	v_cndmask_b32_e32 v136, v136, v137, vcc
	v_rsq_f32_e32 v136, v136
	s_nop 0
	v_mul_f32_e32 v137, 0x45800000, v136
	v_cndmask_b32_e32 v136, v136, v137, vcc
	v_fma_f32 v252, v252, s39, v171
	v_mul_f32_e32 v253, 0x4b800000, v252
	v_cmp_gt_f32_e32 vcc, s40, v252
	s_nop 1
	v_cndmask_b32_e32 v252, v252, v253, vcc
	v_rsq_f32_e32 v252, v252
	s_nop 0
	v_mul_f32_e32 v253, 0x45800000, v252
	v_cndmask_b32_e32 v252, v252, v253, vcc
	v_pk_mul_f32 v[172:173], v[172:173], v[128:129] op_sel_hi:[1,0]
	v_pk_mul_f32 v[174:175], v[174:175], v[128:129] op_sel_hi:[1,0]
	v_pk_mul_f32 v[176:177], v[176:177], v[128:129] op_sel_hi:[1,0]
	v_pk_mul_f32 v[178:179], v[178:179], v[128:129] op_sel_hi:[1,0]
	v_pk_mul_f32 v[180:181], v[180:181], v[128:129] op_sel_hi:[1,0]
	v_pk_mul_f32 v[182:183], v[182:183], v[128:129] op_sel_hi:[1,0]
	v_pk_mul_f32 v[184:185], v[184:185], v[128:129] op_sel_hi:[1,0]
	v_pk_mul_f32 v[186:187], v[186:187], v[128:129] op_sel_hi:[1,0]
	v_pk_mul_f32 v[172:173], v[172:173], v[18:19]
	v_pk_mul_f32 v[174:175], v[174:175], v[20:21]
	v_pk_mul_f32 v[176:177], v[176:177], v[22:23]
	v_pk_mul_f32 v[178:179], v[178:179], v[24:25]
	v_pk_mul_f32 v[180:181], v[180:181], v[26:27]
	v_pk_mul_f32 v[182:183], v[182:183], v[28:29]
	v_pk_mul_f32 v[184:185], v[184:185], v[30:31]
	v_pk_mul_f32 v[186:187], v[186:187], v[32:33]
	s_add_u32 s34, s14, 0x2000000
	s_addc_u32 s35, s15, 0
	global_store_dwordx4 v3, v[172:175], s[34:35] nt
	global_store_dwordx4 v3, v[176:179], s[34:35] offset:1024 nt
	global_store_dwordx4 v3, v[180:183], s[34:35] offset:2048 nt
	global_store_dwordx4 v3, v[184:187], s[34:35] offset:3072 nt
	v_pk_mul_f32 v[188:189], v[188:189], v[132:133] op_sel_hi:[1,0]
	v_pk_mul_f32 v[190:191], v[190:191], v[132:133] op_sel_hi:[1,0]
	v_pk_mul_f32 v[192:193], v[192:193], v[132:133] op_sel_hi:[1,0]
	v_pk_mul_f32 v[194:195], v[194:195], v[132:133] op_sel_hi:[1,0]
	v_pk_mul_f32 v[196:197], v[196:197], v[132:133] op_sel_hi:[1,0]
	v_pk_mul_f32 v[198:199], v[198:199], v[132:133] op_sel_hi:[1,0]
	v_pk_mul_f32 v[200:201], v[200:201], v[132:133] op_sel_hi:[1,0]
	v_pk_mul_f32 v[202:203], v[202:203], v[132:133] op_sel_hi:[1,0]
	v_pk_mul_f32 v[188:189], v[188:189], v[18:19]
	v_pk_mul_f32 v[190:191], v[190:191], v[20:21]
	v_pk_mul_f32 v[192:193], v[192:193], v[22:23]
	v_pk_mul_f32 v[194:195], v[194:195], v[24:25]
	v_pk_mul_f32 v[196:197], v[196:197], v[26:27]
	v_pk_mul_f32 v[198:199], v[198:199], v[28:29]
	v_pk_mul_f32 v[200:201], v[200:201], v[30:31]
	v_pk_mul_f32 v[202:203], v[202:203], v[32:33]
	s_add_u32 s34, s14, 0x2800000
	s_addc_u32 s35, s15, 0
	global_store_dwordx4 v3, v[188:191], s[34:35] nt
	global_store_dwordx4 v3, v[192:195], s[34:35] offset:1024 nt
	global_store_dwordx4 v3, v[196:199], s[34:35] offset:2048 nt
	global_store_dwordx4 v3, v[200:203], s[34:35] offset:3072 nt
	v_pk_mul_f32 v[204:205], v[204:205], v[136:137] op_sel_hi:[1,0]
	v_pk_mul_f32 v[206:207], v[206:207], v[136:137] op_sel_hi:[1,0]
	v_pk_mul_f32 v[208:209], v[208:209], v[136:137] op_sel_hi:[1,0]
	v_pk_mul_f32 v[210:211], v[210:211], v[136:137] op_sel_hi:[1,0]
	v_pk_mul_f32 v[212:213], v[212:213], v[136:137] op_sel_hi:[1,0]
	v_pk_mul_f32 v[214:215], v[214:215], v[136:137] op_sel_hi:[1,0]
	v_pk_mul_f32 v[216:217], v[216:217], v[136:137] op_sel_hi:[1,0]
	v_pk_mul_f32 v[218:219], v[218:219], v[136:137] op_sel_hi:[1,0]
	v_pk_mul_f32 v[204:205], v[204:205], v[18:19]
	v_pk_mul_f32 v[206:207], v[206:207], v[20:21]
	v_pk_mul_f32 v[208:209], v[208:209], v[22:23]
	v_pk_mul_f32 v[210:211], v[210:211], v[24:25]
	v_pk_mul_f32 v[212:213], v[212:213], v[26:27]
	v_pk_mul_f32 v[214:215], v[214:215], v[28:29]
	v_pk_mul_f32 v[216:217], v[216:217], v[30:31]
	v_pk_mul_f32 v[218:219], v[218:219], v[32:33]
	s_add_u32 s34, s14, 0x3000000
	s_addc_u32 s35, s15, 0
	global_store_dwordx4 v3, v[204:207], s[34:35] nt
	global_store_dwordx4 v3, v[208:211], s[34:35] offset:1024 nt
	global_store_dwordx4 v3, v[212:215], s[34:35] offset:2048 nt
	global_store_dwordx4 v3, v[216:219], s[34:35] offset:3072 nt
	v_pk_mul_f32 v[236:237], v[236:237], v[252:253] op_sel_hi:[1,0]
	v_pk_mul_f32 v[238:239], v[238:239], v[252:253] op_sel_hi:[1,0]
	v_pk_mul_f32 v[240:241], v[240:241], v[252:253] op_sel_hi:[1,0]
	v_pk_mul_f32 v[242:243], v[242:243], v[252:253] op_sel_hi:[1,0]
	v_pk_mul_f32 v[244:245], v[244:245], v[252:253] op_sel_hi:[1,0]
	v_pk_mul_f32 v[246:247], v[246:247], v[252:253] op_sel_hi:[1,0]
	v_pk_mul_f32 v[248:249], v[248:249], v[252:253] op_sel_hi:[1,0]
	v_pk_mul_f32 v[250:251], v[250:251], v[252:253] op_sel_hi:[1,0]
	v_pk_mul_f32 v[236:237], v[236:237], v[18:19]
	v_pk_mul_f32 v[238:239], v[238:239], v[20:21]
	v_pk_mul_f32 v[240:241], v[240:241], v[22:23]
	v_pk_mul_f32 v[242:243], v[242:243], v[24:25]
	v_pk_mul_f32 v[244:245], v[244:245], v[26:27]
	v_pk_mul_f32 v[246:247], v[246:247], v[28:29]
	v_pk_mul_f32 v[248:249], v[248:249], v[30:31]
	v_pk_mul_f32 v[250:251], v[250:251], v[32:33]
	s_add_u32 s34, s14, 0x3800000
	s_addc_u32 s35, s15, 0
	global_store_dwordx4 v3, v[236:239], s[34:35] nt
	global_store_dwordx4 v3, v[240:243], s[34:35] offset:1024 nt
	global_store_dwordx4 v3, v[244:247], s[34:35] offset:2048 nt
	global_store_dwordx4 v3, v[248:251], s[34:35] offset:3072 nt
	s_branch .LBB0_2997
